# attention mask LUT as a 16-entry nibble table (128 B, conflict-free): two ds_read_b64 per mask byte, addresses computed just before each read (+6 VALU per step)
# baseline (speedup 1.0000x reference)
;   __device__ __forceinline__ bool next(int i,AttnUnit&u)const{ const int v=vcu+(i>>2)*grid; if(v>=256)return false; const int k=i&3,s=v&7; u.bh=v>>3; u.qb=(k==0)?s:(k==1)?15-s:(k==2)?16+s:31-s; return true; }
; #define REP(n) for (int rep_ = 0; rep_ < 1 + MK_REPN * (((MK_DUP) >> (n)) & 1); ++rep_)
;   AttnUnit u;
;   for(int i=0;S.next(i,u);++i){ S.a_ready(u); attn_unit<THRL>(u.bh/NHEAD,u.bh%NHEAD,u.qb,T.Q,T.K,T.V,T.O,T.MASK,lds); S.done(u); }
; __global__ void __launch_bounds__(NWAVES * 64, 2) mk_fwd(Args args) {
;     ...
;             { const attn_body::AttnTensors AT{(const attn_body::bf16*)(ws + WS_Q), (const attn_body::bf16*)(ws + WS_K), (const attn_body::bf16*)(ws + WS_V), (attn_body::bf16*)(ws + WS_MIX) + 512, (const unsigned*)(ws + (l ? WS_MASK1 : WS_MASK))};
;               const attn_body::StaticOrder S((int)F.G, (int)blockIdx.x);
;               REP(6) attn_body::attn_phase<attn_body::StaticOrder>((char*)lds + RING_OFF, AT, S); }
.LBB0_1258:
	s_andn2_b64 vcc, exec, s[4:5]
	s_cbranch_vccnz .LBB0_1395
	v_mov_b32_e32 v204, 0x3f803f80
	v_mov_b32_e32 v205, 0x3f803f80
	v_mov_b32_e32 v206, 0x3f803f80
	v_mov_b32_e32 v207, 0x3f803f80
	s_mov_b32 s32, 3
	s_mov_b32 s11, 1
	v_lshrrev_b32_e32 v228, 1, v0
	v_and_b32_e32 v229, 1, v0
	v_lshlrev_b32_e32 v230, 2, v229
	v_and_b32_e32 v231, 15, v228
	v_bfe_i32 v232, v231, 0, 1
	v_bfe_i32 v233, v231, 1, 1
	v_and_b32_e32 v232, 0xffff, v232
	v_and_b32_e32 v233, 0xffff0000, v233
	v_or_b32_e32 v232, v232, v233
	v_bfe_i32 v233, v231, 2, 1
	v_bfe_i32 v234, v231, 3, 1
	v_and_b32_e32 v233, 0xffff, v233
	v_and_b32_e32 v234, 0xffff0000, v234
	v_or_b32_e32 v233, v233, v234
	v_lshlrev_b32_e32 v234, 3, v231
	ds_write_b64 v234, v[232:233] offset:51200
	v_mov_b32_e32 v1, v0
	s_mov_b64 s[4:5], s[66:67]
	s_load_dwordx2 s[4:5], s[4:5], 0xd0
	v_readlane_b32 s6, v252, 16
	v_readlane_b32 s7, v252, 17
	s_mov_b32 s55, 0
	s_waitcnt lgkmcnt(0)
	s_add_u32 s8, s4, 0xea00000
	s_addc_u32 s9, s5, 0
	s_add_u32 s17, s4, 0x10a00000
	s_addc_u32 s18, s5, 0
	s_add_u32 s19, s4, 0x12a00000
	s_addc_u32 s20, s5, 0
	s_add_u32 s21, s4, 0x15f00400
	s_addc_u32 s22, s5, 0
	s_add_u32 s23, s4, s6
	s_addc_u32 s54, s5, s7
	s_branch .LBB0_1262

; #define MASK1(p,w,e) ({ unsigned m_; asm("v_bfe_i32 %0, %1, %2, 1":"=v"(m_):"v"(w),"n"(e)); __uint_as_float(__float_as_uint(p)&m_); })
; #define WAIT_BAR(N) asm volatile("s_waitcnt vmcnt(" #N ") lgkmcnt(0)\n\ts_barrier":::"memory")
;   #define DMA_K(t,slot) glds16(ksrc+(long)(t)*KVBLK*DM,(unsigned)__builtin_amdgcn_readfirstlane(kdst+(slot)))
; template<int THRL> __device__ __forceinline__ void attn_unit(int b,int h,int qb,const bf16*Q,const bf16*__restrict__ K,const bf16*__restrict__ V,bf16*O,const unsigned*MASK,char*shm){
;   int tid_=threadIdx.x; asm volatile("":"+v"(tid_));
;   const int tid=tid_,lane=tid&63,r32=lane&31,hi=lane>>5; const int wid=__builtin_amdgcn_readfirstlane(tid>>6);
;   const long rowbase=(long)b*SEQ; const int q0=qb*QB;
;   const bf16*Qw=Q+(rowbase+q0+wid*QBLK)*DM+h*D;
;   const bf16*Kh=K+rowbase*DM+h*D,*Vh=V+rowbase*DM+h*D;
;   const unsigned lds0=(unsigned)(uintptr_t)shm;
;   float*wsf=(float*)(shm+LDS_WS)+wid*64;
;   const bf16*ksrc=Kh+(long)lane*DM+wid*8;
;   const bf16*vsrc=Vh+(long)(16*(wid&3)+(lane>>2))*DM+(wid>>2)*32+(lane&3)*8;
;   const unsigned kdst=lds0+LDS_K+wid*1024, vdst=lds0+LDS_V+wid*1024;
;     ...
;   const int vb0=(int)(lds0+LDS_V)+((lane>>4)&1)*32+(lane&3)*8+(4*hi+((lane&15)>>2))*64;
;   const char*Kbase=shm+LDS_K; bf16x8 kf[8];
;   const lds_cptr shm3=(lds_cptr)shm; const lds_cptr kp0=shm3+LDS_K+hi*1024+r32*16; const lds_cptr vp0=shm3+LDS_V+((lane>>4)&1)*32+(lane&3)*8+(4*hi+((lane&15)>>2))*64;
;   const int NT=(q0+QB)/KVBLK;
;   const unsigned*mwl=MASK+((size_t)(b*256+qb*8+wid)*128)*64+lane;
;   unsigned wA,wB;
;     ...
;   WLOAD(wA,0);WLOAD(wB,1);
;   DMA_K(0,0);DMA_V(0,0);DMA_K(1,SLOTB);
;   bf16x8 qr[4];
;   #pragma unroll
;   for(int d0=0;d0<4;++d0)qr[d0]=*reinterpret_cast<const bf16x8*>(&Qw[(long)r32*DM+d0*16+hi*8]);
;   float mhat=0.f,l_reg=0.f;f32x16 o[2];o[0]=f32x16{};o[1]=f32x16{};f32x16 negm=f32x16{};asm volatile("":"+v"(negm));
;   bool resc=false;
;     ...
;   f32x16 pA0,pA1,pB0,pB1;
;   int sl_prev=0,sl_cur=0,sl_next=SLOTB;
;     ...
;   DMA_K(2,2*SLOTB);
;   WAIT_BAR(3);
;   qkt(pA0,pA1,Kbase,qr,negm,r32,hi);asm volatile("s_nop 15\n\ts_nop 7":"+v"(pA0),"+v"(pA1));
;   START(pA0,pA1);
;   _Pragma("unroll") for(int r=0;r<16;++r)pA1[r]=__builtin_amdgcn_exp2f(pA1[r]);
;   _Pragma("unroll") for(int r=0;r<16;++r){pA0[r]=MASK1(pA0[r],wA,r);pA1[r]=MASK1(pA1[r],wA,16+r);}
.LBB0_1271:
	s_ashr_i32 s4, s6, 31
	s_lshr_b32 s4, s4, 29
	s_add_i32 s4, s6, s4
	s_ashr_i32 s42, s4, 3
	v_mov_b32_e32 v58, v0
	s_and_b32 s4, s4, 0x3fffff8
	s_ashr_i32 s43, s42, 31
	v_readfirstlane_b32 s50, v58
	s_lshl_b32 s51, s56, 8
	s_sub_i32 s38, s6, s4
	s_ashr_i32 s7, s50, 6
	s_lshl_b64 s[4:5], s[42:43], 13
	s_ashr_i32 s39, s51, 31
	s_add_u32 s4, s4, s51
	s_addc_u32 s5, s5, s39
	s_lshl_b32 s39, s7, 5
	s_ashr_i32 s40, s39, 31
	s_add_u32 s44, s4, s39
	s_addc_u32 s45, s5, s40
	s_lshl_b64 s[4:5], s[44:45], 10
	s_add_u32 s40, s8, s4
	s_addc_u32 s41, s9, s5
	s_lshl_b32 s4, s38, 6
	s_ashr_i32 s5, s4, 31
	s_lshl_b64 s[38:39], s[4:5], 1
	s_add_u32 s40, s40, s38
	s_addc_u32 s41, s41, s39
	s_lshl_b64 s[4:5], s[42:43], 23
	s_add_u32 s43, s17, s4
	s_addc_u32 s47, s18, s5
	s_add_u32 s46, s43, s38
	s_addc_u32 s47, s47, s39
	s_add_u32 s4, s19, s4
	v_and_b32_e32 v1, 63, v58
	s_addc_u32 s5, s20, s5
	s_add_u32 s48, s4, s38
	v_lshlrev_b32_e32 v2, 10, v1
	s_addc_u32 s49, s5, s39
	v_lshl_add_u64 v[4:5], s[46:47], 0, v[2:3]
	s_lshl_b32 s46, s7, 3
	s_lshl_b32 s4, s7, 4
	v_bfe_u32 v2, v58, 2, 4
	s_ashr_i32 s47, s46, 31
	v_and_or_b32 v2, s4, 48, v2
	s_ashr_i32 s4, s50, 3
	v_lshl_add_u64 v[194:195], s[46:47], 1, v[4:5]
	s_and_b32 s46, s4, 0xffffffe0
	s_and_b32 s5, s50, 0x3fffffc0
	s_ashr_i32 s47, s46, 31
	s_lshl_b32 s58, s7, 10
	s_cmp_lg_u32 0, -1
	s_cselect_b32 s4, 0, 0
	s_lshl_b32 s42, s42, 8
	s_lshl_b32 s43, s56, 3
	s_add_i32 s42, s42, s43
	s_add_i32 s42, s42, s7
	v_lshlrev_b32_e32 v2, 10, v2
	v_lshlrev_b32_e32 v212, 3, v58
	s_add_i32 s58, s58, s4
	s_ashr_i32 s43, s42, 31
	v_lshl_add_u64 v[4:5], s[48:49], 0, v[2:3]
	v_and_b32_e32 v215, 24, v212
	s_add_i32 s59, s58, 0x6000
	s_add_i32 s4, s51, 0x100
	s_lshl_b64 s[42:43], s[42:43], 15
	v_lshl_add_u64 v[4:5], s[46:47], 1, v[4:5]
	v_lshlrev_b32_e32 v2, 1, v215
	s_add_u32 s42, s23, s42
	v_lshl_add_u64 v[208:209], v[4:5], 0, v[2:3]
	s_addc_u32 s43, s54, s43
	v_lshlrev_b32_e32 v2, 2, v1
	v_lshl_add_u64 v[84:85], s[42:43], 0, v[2:3]
	global_load_dword v59, v[84:85], off
	s_waitcnt vmcnt(0)
	v_and_b32_e32 v225, 0x0f0f0f0f, v59
	v_and_b32_e32 v226, 0xf0f0f0f0, v59
	v_lshl_add_u64 v[186:187], v[84:85], 0, s[30:31]
	global_load_dword v218, v[186:187], off
	v_and_b32_e32 v213, 31, v58
	s_mov_b32 s42, m0
	s_mov_b32 m0, s58
	s_nop 0
	global_load_lds_dwordx4 v[194:195], off
	s_mov_b32 m0, s42
	v_bfe_u32 v214, v58, 5, 1
	s_mov_b32 s42, m0
	s_mov_b32 m0, s59
	s_nop 0
	global_load_lds_dwordx4 v[208:209], off
	s_mov_b32 m0, s42
	v_lshlrev_b32_e32 v2, 10, v213
	v_lshl_add_u64 v[4:5], v[194:195], 0, s[36:37]
	s_add_i32 s42, s58, 0x2000
	s_mov_b32 s43, m0
	s_mov_b32 m0, s42
	s_nop 0
	global_load_lds_dwordx4 v[4:5], off
	s_mov_b32 m0, s43
	v_lshl_or_b32 v2, v214, 4, v2
	global_load_dwordx4 v[138:141], v2, s[40:41]
	global_load_dwordx4 v[134:137], v2, s[40:41] offset:32
	global_load_dwordx4 v[126:129], v2, s[40:41] offset:64
	global_load_dwordx4 v[122:125], v2, s[40:41] offset:96
	v_mov_b32_e32 v228, 0
	v_mov_b32_e32 v229, 0
	v_mov_b32_e32 v230, 0
	v_mov_b32_e32 v231, 0
	v_mov_b32_e32 v232, 0
	v_mov_b32_e32 v233, 0
	v_mov_b32_e32 v234, 0
	v_mov_b32_e32 v235, 0
	v_mov_b32_e32 v236, 0
	v_mov_b32_e32 v237, 0
	v_mov_b32_e32 v238, 0
	v_mov_b32_e32 v239, 0
	v_mov_b32_e32 v240, 0
	v_mov_b32_e32 v241, 0
	v_mov_b32_e32 v242, 0
	v_mov_b32_e32 v243, 0
	v_mov_b32_e32 v16, v3
	v_mov_b32_e32 v17, v3
	v_lshlrev_b32_e32 v2, 10, v214
	v_lshlrev_b32_e32 v18, 4, v213
	v_mov_b32_e32 v4, v3
	v_mov_b32_e32 v5, v3
	v_mov_b32_e32 v6, v3
	v_mov_b32_e32 v7, v3
	v_mov_b32_e32 v8, v3
	v_mov_b32_e32 v9, v3
	v_mov_b32_e32 v10, v3
	v_mov_b32_e32 v11, v3
	v_mov_b32_e32 v12, v3
	v_mov_b32_e32 v13, v3
	v_mov_b32_e32 v14, v3
	v_mov_b32_e32 v15, v3
	v_add3_u32 v221, 0, v2, v18
	v_mov_b32_e32 v2, v3
	v_mov_b64_e32 v[32:33], v[16:17]
	v_mov_b64_e32 v[30:31], v[14:15]
	v_mov_b64_e32 v[28:29], v[12:13]
	v_mov_b64_e32 v[26:27], v[10:11]
	v_mov_b64_e32 v[24:25], v[8:9]
	v_mov_b64_e32 v[22:23], v[6:7]
	v_mov_b64_e32 v[20:21], v[4:5]
	v_mov_b64_e32 v[18:19], v[2:3]
	v_lshl_add_u64 v[34:35], v[194:195], 0, s[0:1]
	s_add_i32 s40, s58, 0x4000
	s_mov_b32 s41, m0
	s_mov_b32 m0, s40
	s_nop 0
	global_load_lds_dwordx4 v[34:35], off
	s_mov_b32 m0, s41
	s_waitcnt vmcnt(3) lgkmcnt(0)
	s_barrier
	ds_read_b128 v[50:53], v221
	ds_read_b128 v[54:57], v221 offset:512
	s_mov_b32 s40, 0xf149f2ca
	s_waitcnt vmcnt(3) lgkmcnt(1)
	v_mfma_f32_32x32x16_bf16 v[34:49], v[50:53], v[138:141], v[18:33]
	v_bfe_i32 v70, v59, 3, 1
	v_bfe_i32 v71, v59, 4, 1
	v_bfe_i32 v72, v59, 5, 1
	v_bfe_i32 v73, v59, 6, 1
	v_bfe_i32 v74, v59, 7, 1
	v_bfe_i32 v75, v59, 8, 1
	v_bfe_i32 v76, v59, 9, 1
	s_waitcnt lgkmcnt(0)
	v_mfma_f32_32x32x16_bf16 v[18:33], v[54:57], v[138:141], v[18:33]
	ds_read_b128 v[50:53], v221 offset:2048
	ds_read_b128 v[54:57], v221 offset:2560
	v_bfe_i32 v77, v59, 10, 1
	v_bfe_i32 v78, v59, 11, 1
	v_bfe_i32 v79, v59, 12, 1
	v_bfe_i32 v80, v59, 13, 1
	v_bfe_i32 v81, v59, 14, 1
	v_bfe_i32 v82, v59, 15, 1
	s_waitcnt vmcnt(2) lgkmcnt(1)
	v_mfma_f32_32x32x16_bf16 v[34:49], v[50:53], v[134:137], v[34:49]
	s_lshl_b32 s5, s5, 2
	v_bfe_i32 v86, v59, 16, 1
	v_bfe_i32 v87, v59, 17, 1
	v_bfe_i32 v69, v59, 2, 1
	s_ashr_i32 s61, s4, 6
	s_add_i32 s57, s5, 0
	v_bfe_i32 v67, v59, 0, 1
	s_waitcnt lgkmcnt(0)
	v_mfma_f32_32x32x16_bf16 v[18:33], v[54:57], v[134:137], v[18:33]
	ds_read_b128 v[50:53], v221 offset:4096
	ds_read_b128 v[54:57], v221 offset:4608
	v_bfe_i32 v68, v59, 1, 1
	s_mov_b32 s92, 1
	s_mov_b32 s48, 0
	s_movk_i32 s60, 0x2000
	s_movk_i32 s62, 0x4000
	v_bfe_i32 v88, v59, 18, 1
	s_waitcnt vmcnt(1) lgkmcnt(1)
; #define MASK1(p,w,e) ({ unsigned m_; asm("v_bfe_i32 %0, %1, %2, 1":"=v"(m_):"v"(w),"n"(e)); __uint_as_float(__float_as_uint(p)&m_); })
; #define WAIT_BAR(N) asm volatile("s_waitcnt vmcnt(" #N ") lgkmcnt(0)\n\ts_barrier":::"memory")
;   #define DMA_K(t,slot) glds16(ksrc+(long)(t)*KVBLK*DM,(unsigned)__builtin_amdgcn_readfirstlane(kdst+(slot)))
;   #define DMA_V(t,slot) glds16(vsrc+(long)(t)*KVBLK*DM,(unsigned)__builtin_amdgcn_readfirstlane(vdst+(slot)))
;   #define ROT() do{sl_prev=sl_cur;sl_cur=sl_next;sl_next=(sl_next==(NSLOT-1)*SLOTB)?0:sl_next+SLOTB;}while(0)
; template<int THRL> __device__ __forceinline__ void attn_unit(int b,int h,int qb,const bf16*Q,const bf16*__restrict__ K,const bf16*__restrict__ V,bf16*O,const unsigned*MASK,char*shm){
;     ...
;   qkt(pA0,pA1,Kbase,qr,negm,r32,hi);asm volatile("s_nop 15\n\ts_nop 7":"+v"(pA0),"+v"(pA1));
;   START(pA0,pA1);
;   _Pragma("unroll") for(int r=0;r<16;++r)pA1[r]=__builtin_amdgcn_exp2f(pA1[r]);
;   _Pragma("unroll") for(int r=0;r<16;++r){pA0[r]=MASK1(pA0[r],wA,r);pA1[r]=MASK1(pA1[r],wA,16+r);}
;   WAIT_BAR(0);
;   DMA_K(3,0);DMA_V(1,SLOTB);
;   ROT();
;   kload8(kf,kp0+sl_cur);
;   WAIT_BAR(2);
;   s16x4 vlo[8],vhi[8]; u32x4 pw0,pw1,pw2,pw3;
	v_mfma_f32_32x32x16_bf16 v[34:49], v[50:53], v[126:129], v[34:49]
	ds_read_b128 v[50:53], v221 offset:6144
	v_bfe_i32 v89, v59, 19, 1
	v_bfe_i32 v90, v59, 20, 1
	v_bfe_i32 v91, v59, 21, 1
	v_bfe_i32 v92, v59, 22, 1
	v_bfe_i32 v93, v59, 23, 1
	v_bfe_i32 v94, v59, 24, 1
	s_waitcnt lgkmcnt(1)
	v_mfma_f32_32x32x16_bf16 v[18:33], v[54:57], v[126:129], v[18:33]
	ds_read_b128 v[54:57], v221 offset:6656
	v_bfe_i32 v95, v59, 25, 1
	v_bfe_i32 v96, v59, 26, 1
	v_bfe_i32 v97, v59, 27, 1
	v_bfe_i32 v98, v59, 28, 1
	v_bfe_i32 v99, v59, 29, 1
	v_bfe_i32 v100, v59, 30, 1
	s_waitcnt vmcnt(0) lgkmcnt(1)
	v_mfma_f32_32x32x16_bf16 v[34:49], v[50:53], v[122:125], v[34:49]
	v_lshlrev_b32_e32 v50, 1, v58
	v_lshlrev_b32_e32 v51, 4, v58
	v_and_b32_e32 v217, 32, v50
	v_and_b32_e32 v50, 0xc0, v51
	v_lshl_or_b32 v216, v214, 8, v50
	v_add_u32_e32 v50, 0, v217
	v_add3_u32 v220, v50, v215, v216
	s_waitcnt lgkmcnt(0)
	v_mfma_f32_32x32x16_bf16 v[18:33], v[54:57], v[122:125], v[18:33]
	s_nop 15
	s_nop 7
	s_nop 0
	v_max3_f32 v50, v34, v35, v18
	v_max3_f32 v51, v36, v37, v19
	s_nop 0
	v_max3_f32 v50, v50, v20, v21
	v_max3_f32 v51, v51, v40, v41
	s_nop 0
	v_max3_f32 v50, v50, v38, v39
	v_max3_f32 v51, v51, v24, v25
	s_nop 0
	v_max3_f32 v50, v50, v22, v23
	v_max3_f32 v51, v51, v44, v45
	s_nop 0
	v_max3_f32 v50, v50, v42, v43
	v_max3_f32 v51, v51, v28, v29
	s_nop 0
	v_max3_f32 v50, v50, v26, v27
	v_max3_f32 v51, v51, v48, v49
	s_nop 0
	v_max3_f32 v50, v50, v46, v47
	v_max3_f32 v51, v51, v32, v33
	s_nop 0
	v_max3_f32 v50, v50, v30, v31
	s_nop 0
	v_max_f32_e32 v50, v50, v51
	s_nop 0
	v_mov_b32_e32 v51, v50
	s_nop 1
	v_permlane32_swap_b32_e32 v50, v51
	v_max_f32_e32 v50, v50, v51
	s_nop 0
	v_cmp_lt_f32_e32 vcc, s40, v50
	v_cmp_gt_u32_e64 s[40:41], 32, v1
	s_nop 0
	v_cndmask_b32_e32 v50, 0, v50, vcc
	v_sub_f32_e32 v18, v18, v50
	v_sub_f32_e32 v19, v19, v50
	v_sub_f32_e32 v52, v36, v50
	v_sub_f32_e32 v53, v37, v50
	v_sub_f32_e32 v54, v38, v50
	v_sub_f32_e32 v55, v39, v50
	v_sub_f32_e32 v56, v40, v50
	v_sub_f32_e32 v57, v41, v50
	v_sub_f32_e32 v58, v42, v50
	v_sub_f32_e32 v60, v43, v50
	v_sub_f32_e32 v61, v44, v50
	v_sub_f32_e32 v62, v45, v50
	v_sub_f32_e32 v63, v46, v50
	v_sub_f32_e32 v64, v47, v50
	v_sub_f32_e32 v65, v48, v50
	v_sub_f32_e32 v66, v49, v50
	s_nop 0
	v_exp_f32_e32 v52, v52
	v_exp_f32_e32 v53, v53
	v_exp_f32_e32 v54, v54
	v_exp_f32_e32 v55, v55
	v_exp_f32_e32 v56, v56
	v_exp_f32_e32 v57, v57
	v_exp_f32_e32 v58, v58
	v_exp_f32_e32 v60, v60
	v_exp_f32_e32 v61, v61
	v_exp_f32_e32 v62, v62
	v_exp_f32_e32 v63, v63
	v_exp_f32_e32 v64, v64
	v_exp_f32_e32 v65, v65
	v_exp_f32_e32 v66, v66
	v_exp_f32_e32 v18, v18
	v_exp_f32_e32 v19, v19
	v_add_f32_e32 v219, v3, v50
	v_sub_f32_e32 v34, v34, v50
	v_sub_f32_e32 v35, v35, v50
	v_sub_f32_e32 v20, v20, v50
	v_sub_f32_e32 v21, v21, v50
	v_sub_f32_e32 v22, v22, v50
	s_nop 0
	v_xor_b32_e32 v36, 0x80000000, v219
	v_sub_f32_e32 v23, v23, v50
	v_sub_f32_e32 v24, v24, v50
	v_sub_f32_e32 v25, v25, v50
	v_sub_f32_e32 v26, v26, v50
	v_sub_f32_e32 v27, v27, v50
	v_sub_f32_e32 v28, v28, v50
	v_sub_f32_e32 v29, v29, v50
	v_sub_f32_e32 v30, v30, v50
	v_sub_f32_e32 v31, v31, v50
	v_sub_f32_e32 v32, v32, v50
	v_sub_f32_e32 v33, v33, v50
	v_mov_b32_e32 v37, v36
	v_mov_b32_e32 v38, v36
	v_mov_b32_e32 v39, v36
	v_mov_b32_e32 v40, v36
	v_mov_b32_e32 v41, v36
	v_mov_b32_e32 v42, v36
	v_mov_b32_e32 v43, v36
	v_mov_b32_e32 v44, v36
	v_mov_b32_e32 v45, v36
	v_mov_b32_e32 v46, v36
	v_mov_b32_e32 v47, v36
	v_mov_b32_e32 v48, v36
	v_mov_b32_e32 v49, v36
	v_mov_b32_e32 v50, v36
	v_mov_b32_e32 v51, v36
	s_waitcnt vmcnt(0) lgkmcnt(0)
	s_barrier
	v_and_b32_e32 v83, v82, v66
	v_and_b32_e32 v82, v81, v65
	v_and_b32_e32 v81, v80, v64
	v_and_b32_e32 v80, v79, v63
	v_and_b32_e32 v79, v78, v62
	v_and_b32_e32 v78, v77, v61
	v_and_b32_e32 v77, v76, v60
	v_and_b32_e32 v76, v75, v58
	v_and_b32_e32 v75, v74, v57
	v_and_b32_e32 v74, v73, v56
	v_and_b32_e32 v73, v72, v55
	v_and_b32_e32 v72, v71, v54
	v_and_b32_e32 v71, v70, v53
	v_and_b32_e32 v70, v69, v52
	v_and_b32_e32 v53, v87, v19
	v_and_b32_e32 v52, v86, v18
	v_lshl_add_u64 v[18:19], v[194:195], 0, s[82:83]
	s_mov_b32 s4, m0
	s_mov_b32 m0, s58
	s_nop 0
	global_load_lds_dwordx4 v[18:19], off
	s_mov_b32 m0, s4
	v_lshl_add_u64 v[18:19], v[208:209], 0, s[36:37]
	s_add_i32 s4, s58, 0x8000
	s_mov_b32 s5, m0
	s_mov_b32 m0, s4
	s_nop 0
	global_load_lds_dwordx4 v[18:19], off
	s_mov_b32 m0, s5
	ds_read_b128 v[178:181], v221 offset:8192
	ds_read_b128 v[170:173], v221 offset:8704
	ds_read_b128 v[174:177], v221 offset:10240
	ds_read_b128 v[162:165], v221 offset:10752
	ds_read_b128 v[166:169], v221 offset:12288
	ds_read_b128 v[154:157], v221 offset:12800
	ds_read_b128 v[158:161], v221 offset:14336
	ds_read_b128 v[150:153], v221 offset:14848
	v_exp_f32_e32 v34, v34
	v_exp_f32_e32 v35, v35
	v_exp_f32_e32 v20, v20
	v_exp_f32_e32 v21, v21
	v_exp_f32_e32 v22, v22
	v_exp_f32_e32 v23, v23
	v_exp_f32_e32 v24, v24
	v_exp_f32_e32 v25, v25
	v_exp_f32_e32 v26, v26
	v_exp_f32_e32 v27, v27
	v_exp_f32_e32 v28, v28
	v_exp_f32_e32 v29, v29
	v_exp_f32_e32 v30, v30
	v_exp_f32_e32 v31, v31
	v_exp_f32_e32 v32, v32
	v_exp_f32_e32 v33, v33
	s_waitcnt vmcnt(2) lgkmcnt(0)
	s_barrier
	v_and_b32_e32 v69, v68, v35
	v_and_b32_e32 v68, v67, v34
	v_bfe_i32 v34, v59, 31, 1
	v_and_b32_e32 v66, v100, v32
	v_and_b32_e32 v67, v34, v33
	v_and_b32_e32 v65, v99, v31
	v_and_b32_e32 v64, v98, v30
	v_and_b32_e32 v63, v97, v29
	v_and_b32_e32 v62, v96, v28
	v_and_b32_e32 v61, v95, v27
	v_and_b32_e32 v60, v94, v26
	v_and_b32_e32 v59, v93, v25
	v_and_b32_e32 v58, v92, v24
	v_and_b32_e32 v57, v91, v23
	v_and_b32_e32 v56, v90, v22
	v_and_b32_e32 v55, v89, v21
	v_and_b32_e32 v54, v88, v20
	s_cmp_lt_i32 s61, 7
	s_cbranch_scc1 .LBB0_1287
	s_mov_b64 s[4:5], 0x50000
	v_lshlrev_b32_e32 v18, 4, v214
	v_lshl_add_u64 v[188:189], v[194:195], 0, s[4:5]
	s_mov_b64 s[4:5], 0x300
	v_mov_b64_e32 v[34:35], v[16:17]
	v_lshl_add_u64 v[192:193], v[84:85], 0, s[4:5]
	v_add_u32_e32 v85, s57, v18
	v_mov_b64_e32 v[32:33], v[14:15]
	v_mov_b64_e32 v[30:31], v[12:13]
	v_mov_b64_e32 v[28:29], v[10:11]
	v_mov_b64_e32 v[26:27], v[8:9]
	v_mov_b64_e32 v[24:25], v[6:7]
	v_mov_b64_e32 v[22:23], v[4:5]
	v_mov_b64_e32 v[20:21], v[2:3]
	v_mov_b64_e32 v[18:19], v[16:17]
	s_add_i32 s46, s61, -5
	v_lshl_add_u32 v210, v213, 2, s57
	v_lshl_add_u64 v[190:191], v[208:209], 0, s[82:83]
	s_mov_b32 s4, 0
	s_movk_i32 s48, 0x4000
	s_movk_i32 s47, 0x2000
	v_mov_b32_e32 v84, 0
	v_mov_b64_e32 v[16:17], v[14:15]
	v_mov_b64_e32 v[14:15], v[12:13]
	v_mov_b64_e32 v[12:13], v[10:11]
	v_mov_b64_e32 v[10:11], v[8:9]
	v_mov_b64_e32 v[8:9], v[6:7]
	v_mov_b64_e32 v[6:7], v[4:5]
	v_mov_b64_e32 v[4:5], v[2:3]
.LBB0_1273:
	s_movk_i32 s42, 0xff00
	s_mov_b32 s43, -1
	v_lshl_add_u64 v[86:87], v[192:193], 0, s[42:43]
	v_lshl_add_u64 v[222:223], v[188:189], 0, s[86:87]
	s_add_i32 s63, s47, s58
	s_mov_b32 m0, s63
	s_nop 0
	global_load_lds_dwordx4 v[222:223], off
	v_lshl_add_u64 v[222:223], v[190:191], 0, s[86:87]
	s_add_i32 s63, s48, s59
	s_mov_b32 m0, s63
	s_nop 0
	global_load_lds_dwordx4 v[222:223], off
	global_load_dword v2, v[86:87], off
	v_add_u32_e32 v255, s4, v220
	ds_read_b64_tr_b16 v[182:183], v255 offset:24576
	ds_read_b64_tr_b16 v[184:185], v255 offset:25088
	s_waitcnt lgkmcnt(9)
	v_mfma_f32_32x32x16_bf16 v[102:117], v[178:181], v[138:141], v[36:51]
	v_cvt_pk_bf16_f32 v146, v68, v69
	v_cvt_pk_bf16_f32 v147, v70, v71
	ds_read_b64_tr_b16 v[178:179], v255 offset:28672
	ds_read_b64_tr_b16 v[180:181], v255 offset:29184
	s_waitcnt lgkmcnt(10)
	v_mfma_f32_32x32x16_bf16 v[86:101], v[170:173], v[138:141], v[36:51]
	v_cvt_pk_bf16_f32 v148, v72, v73
	v_cvt_pk_bf16_f32 v149, v74, v75
	ds_read_b64_tr_b16 v[170:171], v255 offset:25600
	ds_read_b64_tr_b16 v[172:173], v255 offset:26112
	s_waitcnt lgkmcnt(11)
	v_mfma_f32_32x32x16_bf16 v[102:117], v[174:177], v[134:137], v[102:117]
	v_cvt_pk_bf16_f32 v142, v76, v77
	v_cvt_pk_bf16_f32 v143, v78, v79
	ds_read_b64_tr_b16 v[76:77], v255 offset:29696
	ds_read_b64_tr_b16 v[78:79], v255 offset:30208
	s_waitcnt lgkmcnt(12)
	v_mfma_f32_32x32x16_bf16 v[86:101], v[162:165], v[134:137], v[86:101]
	v_cvt_pk_bf16_f32 v144, v80, v81
	v_cvt_pk_bf16_f32 v145, v82, v83
	ds_read_b64_tr_b16 v[72:73], v255 offset:26624
	ds_read_b64_tr_b16 v[74:75], v255 offset:27136
	s_waitcnt lgkmcnt(13)
	v_mfma_f32_32x32x16_bf16 v[102:117], v[166:169], v[126:129], v[102:117]
	v_cvt_pk_bf16_f32 v130, v52, v53
	v_cvt_pk_bf16_f32 v131, v54, v55
	ds_read_b64_tr_b16 v[68:69], v255 offset:30720
	ds_read_b64_tr_b16 v[70:71], v255 offset:31232
	s_waitcnt lgkmcnt(14)
	v_mfma_f32_32x32x16_bf16 v[86:101], v[154:157], v[126:129], v[86:101]
	v_cvt_pk_bf16_f32 v132, v56, v57
	v_cvt_pk_bf16_f32 v133, v58, v59
	ds_read_b64_tr_b16 v[56:57], v255 offset:27648
	ds_read_b64_tr_b16 v[58:59], v255 offset:28160
	s_waitcnt lgkmcnt(14)
	v_mfma_f32_32x32x16_bf16 v[102:117], v[158:161], v[122:125], v[102:117]
	v_cvt_pk_bf16_f32 v118, v60, v61
	v_cvt_pk_bf16_f32 v119, v62, v63
	ds_read_b64_tr_b16 v[52:53], v255 offset:31744
	ds_read_b64_tr_b16 v[54:55], v255 offset:32256
	v_mfma_f32_32x32x16_bf16 v[86:101], v[150:153], v[122:125], v[86:101]
	v_cvt_pk_bf16_f32 v120, v64, v65
	v_cvt_pk_bf16_f32 v121, v66, v67
	v_lshlrev_b32_sdwa v248, s32, v225 dst_sel:DWORD dst_unused:UNUSED_PAD src0_sel:DWORD src1_sel:BYTE_0
	v_lshrrev_b32_sdwa v249, s11, v226 dst_sel:DWORD dst_unused:UNUSED_PAD src0_sel:DWORD src1_sel:BYTE_0
	ds_read_b64 v[80:81], v248 offset:51200
	ds_read_b64 v[82:83], v249 offset:51200
	v_max_f32_e32 v60, v103, v103
	v_max_f32_e32 v61, v102, v102
	v_max_f32_e32 v60, v61, v60
	v_max3_f32 v61, v104, v105, v87
	v_max3_f32 v60, v60, v86, v88
	v_max3_f32 v60, v60, v89, v106
	v_max3_f32 v61, v61, v108, v109
	v_max3_f32 v60, v60, v107, v90
	v_max3_f32 v61, v61, v92, v93
	v_max3_f32 v60, v60, v91, v110
	v_max3_f32 v61, v61, v112, v113
	v_max3_f32 v60, v60, v111, v94
	v_max3_f32 v61, v61, v96, v97
	v_max3_f32 v60, v60, v95, v114
	v_max3_f32 v61, v61, v116, v117
	v_max3_f32 v60, v60, v115, v98
	v_max3_f32 v61, v61, v100, v101
	v_max3_f32 v60, v60, v99, v61
	v_mov_b32_e32 v61, v60
	s_nop 1
	v_permlane32_swap_b32_e32 v60, v61
	v_max_f32_e32 v61, v61, v61
	v_max_f32_e32 v60, v60, v60
	v_max_f32_e32 v60, v60, v61
	v_cmp_lt_f32_e32 vcc, s14, v60
	s_cmp_lg_u64 vcc, 0
	s_cselect_b64 s[42:43], -1, 0
	s_cbranch_vccnz .LBB0_1281
.LBB0_1274:
	s_waitcnt lgkmcnt(0)
	v_and_b32_e32 v146, v146, v80
	v_and_b32_e32 v147, v147, v81
	v_and_b32_e32 v148, v148, v82
	v_and_b32_e32 v149, v149, v83
	v_lshlrev_b32_sdwa v248, s32, v225 dst_sel:DWORD dst_unused:UNUSED_PAD src0_sel:DWORD src1_sel:BYTE_1
	v_lshrrev_b32_sdwa v249, s11, v226 dst_sel:DWORD dst_unused:UNUSED_PAD src0_sel:DWORD src1_sel:BYTE_1
	ds_read_b64 v[80:81], v248 offset:51200
	ds_read_b64 v[82:83], v249 offset:51200
	s_waitcnt lgkmcnt(14)
	v_mfma_f32_32x32x16_bf16 v[20:35], v[146:149], v[182:185], v[20:35]
	v_exp_f32_e32 v102, v102
	v_exp_f32_e32 v103, v103
	v_exp_f32_e32 v104, v104
	v_exp_f32_e32 v105, v105
	s_waitcnt lgkmcnt(12)
	v_mfma_f32_32x32x16_bf16 v[4:19], v[146:149], v[178:181], v[4:19]
	v_mfma_f32_32x32x16_bf16 v[228:243], v[146:149], v[204:207], v[228:243]
	v_exp_f32_e32 v106, v106
	v_exp_f32_e32 v107, v107
	v_exp_f32_e32 v108, v108
	v_exp_f32_e32 v109, v109
	s_waitcnt lgkmcnt(0)
	v_and_b32_e32 v142, v142, v80
	v_and_b32_e32 v143, v143, v81
	v_and_b32_e32 v144, v144, v82
	v_and_b32_e32 v145, v145, v83
	v_lshlrev_b32_sdwa v248, s32, v225 dst_sel:DWORD dst_unused:UNUSED_PAD src0_sel:DWORD src1_sel:BYTE_2
	v_lshrrev_b32_sdwa v249, s11, v226 dst_sel:DWORD dst_unused:UNUSED_PAD src0_sel:DWORD src1_sel:BYTE_2
	ds_read_b64 v[80:81], v248 offset:51200
	ds_read_b64 v[82:83], v249 offset:51200
	v_add_u32_e32 v64, s48, v221
	ds_read_b128 v[60:63], v64
	ds_read_b128 v[150:153], v64 offset:512
	s_waitcnt lgkmcnt(12)
	v_mfma_f32_32x32x16_bf16 v[20:35], v[142:145], v[170:173], v[20:35]
	v_exp_f32_e32 v110, v110
	v_exp_f32_e32 v111, v111
	v_exp_f32_e32 v112, v112
	v_exp_f32_e32 v113, v113
	ds_read_b128 v[174:177], v64 offset:2048
	ds_read_b128 v[162:165], v64 offset:2560
	s_waitcnt lgkmcnt(12)
	v_mfma_f32_32x32x16_bf16 v[4:19], v[142:145], v[76:79], v[4:19]
	v_mfma_f32_32x32x16_bf16 v[228:243], v[142:145], v[204:207], v[228:243]
	v_exp_f32_e32 v114, v114
	v_exp_f32_e32 v115, v115
	v_exp_f32_e32 v116, v116
	v_exp_f32_e32 v117, v117
	s_waitcnt lgkmcnt(4)
; #define WAIT_BAR(N) asm volatile("s_waitcnt vmcnt(" #N ") lgkmcnt(0)\n\ts_barrier":::"memory")
;   #define RESC() do{ if(resc){ asm volatile("s_waitcnt lgkmcnt(0)":::"memory"); \
;       _Pragma("unroll") for(int d_=0;d_<2;++d_) _Pragma("unroll") for(int r=0;r<16;++r)o[d_][r]*=wsf[crow(r,hi)]; } }while(0)
;   #define ROT() do{sl_prev=sl_cur;sl_cur=sl_next;sl_next=(sl_next==(NSLOT-1)*SLOTB)?0:sl_next+SLOTB;}while(0)
; template<int THRL> __device__ __forceinline__ void attn_unit(int b,int h,int qb,const bf16*Q,const bf16*__restrict__ K,const bf16*__restrict__ V,bf16*O,const unsigned*MASK,char*shm){
;     ...
;   int t=1;
;   for(;t+5<NT;t+=2){
;     STEP(pB0,pB1,pA0,pA1,t,true,true,true,wB,wA);     WAIT_BAR(2); RESC(); ROT();
	v_and_b32_e32 v130, v130, v80
	v_and_b32_e32 v131, v131, v81
	v_and_b32_e32 v132, v132, v82
	v_and_b32_e32 v133, v133, v83
	v_lshlrev_b32_sdwa v248, s32, v225 dst_sel:DWORD dst_unused:UNUSED_PAD src0_sel:DWORD src1_sel:BYTE_3
	v_lshrrev_b32_sdwa v249, s11, v226 dst_sel:DWORD dst_unused:UNUSED_PAD src0_sel:DWORD src1_sel:BYTE_3
	ds_read_b64 v[80:81], v248 offset:51200
	ds_read_b64 v[82:83], v249 offset:51200
	ds_read_b128 v[170:173], v64 offset:4096
	ds_read_b128 v[158:161], v64 offset:4608
	s_waitcnt lgkmcnt(12)
	v_mfma_f32_32x32x16_bf16 v[20:35], v[130:133], v[72:75], v[20:35]
	v_exp_f32_e32 v86, v86
	v_exp_f32_e32 v87, v87
	v_exp_f32_e32 v88, v88
	v_exp_f32_e32 v89, v89
	ds_read_b128 v[166:169], v64 offset:6144
	ds_read_b128 v[154:157], v64 offset:6656
	s_waitcnt lgkmcnt(12)
	v_mfma_f32_32x32x16_bf16 v[4:19], v[130:133], v[68:71], v[4:19]
	v_mfma_f32_32x32x16_bf16 v[228:243], v[130:133], v[204:207], v[228:243]
	v_exp_f32_e32 v90, v90
	v_exp_f32_e32 v91, v91
	v_exp_f32_e32 v92, v92
	v_exp_f32_e32 v93, v93
	s_waitcnt lgkmcnt(4)
	v_and_b32_e32 v118, v118, v80
	v_and_b32_e32 v119, v119, v81
	v_and_b32_e32 v120, v120, v82
	v_and_b32_e32 v121, v121, v83
	s_nop 0
	s_waitcnt lgkmcnt(10)
	v_mfma_f32_32x32x16_bf16 v[20:35], v[118:121], v[56:59], v[20:35]
	v_exp_f32_e32 v94, v94
	v_exp_f32_e32 v95, v95
	v_exp_f32_e32 v96, v96
	v_exp_f32_e32 v97, v97
	s_waitcnt lgkmcnt(8)
	v_mfma_f32_32x32x16_bf16 v[4:19], v[118:121], v[52:55], v[4:19]
	v_mfma_f32_32x32x16_bf16 v[228:243], v[118:121], v[204:207], v[228:243]
	v_exp_f32_e32 v98, v98
	v_exp_f32_e32 v99, v99
	v_exp_f32_e32 v100, v100
	v_exp_f32_e32 v101, v101
	s_waitcnt vmcnt(3)
	v_and_b32_e32 v225, 0x0f0f0f0f, v218
	v_and_b32_e32 v226, 0xf0f0f0f0, v218
	s_waitcnt vmcnt(3) lgkmcnt(0)
	s_barrier
	s_andn2_b64 vcc, exec, s[42:43]
	s_cbranch_vccnz .LBB0_1276
	s_waitcnt lgkmcnt(0)
	ds_read_b128 v[52:55], v85 offset:49248
	ds_read_b128 v[56:59], v85 offset:49216
	ds_read_b128 v[64:67], v85 offset:49184
	ds_read_b128 v[68:71], v85 offset:49152
	s_waitcnt lgkmcnt(3)
	v_pk_mul_f32 v[32:33], v[32:33], v[52:53]
	s_waitcnt lgkmcnt(2)
	v_pk_mul_f32 v[28:29], v[28:29], v[56:57]
	s_waitcnt lgkmcnt(1)
	v_pk_mul_f32 v[24:25], v[24:25], v[64:65]
	v_pk_mul_f32 v[34:35], v[34:35], v[54:55]
	v_pk_mul_f32 v[30:31], v[30:31], v[58:59]
	v_pk_mul_f32 v[26:27], v[26:27], v[66:67]
	s_waitcnt lgkmcnt(0)
	v_pk_mul_f32 v[22:23], v[22:23], v[70:71]
	v_pk_mul_f32 v[20:21], v[20:21], v[68:69]
	v_pk_mul_f32 v[16:17], v[16:17], v[52:53]
	v_pk_mul_f32 v[12:13], v[12:13], v[56:57]
	v_pk_mul_f32 v[8:9], v[8:9], v[64:65]
	v_pk_mul_f32 v[18:19], v[18:19], v[54:55]
	v_pk_mul_f32 v[14:15], v[14:15], v[58:59]
	v_pk_mul_f32 v[10:11], v[10:11], v[66:67]
	v_pk_mul_f32 v[6:7], v[6:7], v[70:71]
	v_pk_mul_f32 v[4:5], v[4:5], v[68:69]
	v_pk_mul_f32 v[240:241], v[240:241], v[52:53]
	v_pk_mul_f32 v[236:237], v[236:237], v[56:57]
	v_pk_mul_f32 v[232:233], v[232:233], v[64:65]
	v_pk_mul_f32 v[242:243], v[242:243], v[54:55]
	v_pk_mul_f32 v[238:239], v[238:239], v[58:59]
	v_pk_mul_f32 v[234:235], v[234:235], v[66:67]
	v_pk_mul_f32 v[230:231], v[230:231], v[70:71]
	v_pk_mul_f32 v[228:229], v[228:229], v[68:69]
.LBB0_1276:
	s_add_i32 s4, s48, 0x2000
	s_cmpk_lg_i32 s48, 0x4000
	s_cselect_b32 s60, s4, 0
	s_add_i32 s63, s48, s58
	s_mov_b32 m0, s63
	s_nop 0
	global_load_lds_dwordx4 v[188:189], off
	s_add_i32 s63, s60, s59
	s_mov_b32 m0, s63
	s_nop 0
	global_load_lds_dwordx4 v[190:191], off
	global_load_dword v218, v[192:193], off
	v_add_u32_e32 v255, s47, v220
	ds_read_b64_tr_b16 v[182:183], v255 offset:24576
	ds_read_b64_tr_b16 v[184:185], v255 offset:25088
	s_waitcnt lgkmcnt(9)
	v_mfma_f32_32x32x16_bf16 v[68:83], v[60:63], v[138:141], v[36:51]
	v_cvt_pk_bf16_f32 v146, v102, v103
	v_cvt_pk_bf16_f32 v147, v104, v105
	ds_read_b64_tr_b16 v[178:179], v255 offset:28672
	ds_read_b64_tr_b16 v[180:181], v255 offset:29184
	s_waitcnt lgkmcnt(10)
	v_mfma_f32_32x32x16_bf16 v[52:67], v[150:153], v[138:141], v[36:51]
	v_cvt_pk_bf16_f32 v148, v106, v107
	v_cvt_pk_bf16_f32 v149, v108, v109
	ds_read_b64_tr_b16 v[150:151], v255 offset:25600
	ds_read_b64_tr_b16 v[152:153], v255 offset:26112
	s_waitcnt lgkmcnt(11)
	v_mfma_f32_32x32x16_bf16 v[68:83], v[174:177], v[134:137], v[68:83]
	v_cvt_pk_bf16_f32 v142, v110, v111
	v_cvt_pk_bf16_f32 v143, v112, v113
	ds_read_b64_tr_b16 v[110:111], v255 offset:29696
	ds_read_b64_tr_b16 v[112:113], v255 offset:30208
	s_waitcnt lgkmcnt(12)
	v_mfma_f32_32x32x16_bf16 v[52:67], v[162:165], v[134:137], v[52:67]
	v_cvt_pk_bf16_f32 v144, v114, v115
	v_cvt_pk_bf16_f32 v145, v116, v117
	ds_read_b64_tr_b16 v[106:107], v255 offset:26624
	ds_read_b64_tr_b16 v[108:109], v255 offset:27136
	s_waitcnt lgkmcnt(13)
	v_mfma_f32_32x32x16_bf16 v[68:83], v[170:173], v[126:129], v[68:83]
	v_cvt_pk_bf16_f32 v130, v86, v87
	v_cvt_pk_bf16_f32 v131, v88, v89
	ds_read_b64_tr_b16 v[102:103], v255 offset:30720
	ds_read_b64_tr_b16 v[104:105], v255 offset:31232
	s_waitcnt lgkmcnt(14)
	v_mfma_f32_32x32x16_bf16 v[52:67], v[158:161], v[126:129], v[52:67]
	v_cvt_pk_bf16_f32 v132, v90, v91
	v_cvt_pk_bf16_f32 v133, v92, v93
	ds_read_b64_tr_b16 v[90:91], v255 offset:27648
	ds_read_b64_tr_b16 v[92:93], v255 offset:28160
	s_waitcnt lgkmcnt(14)
	v_mfma_f32_32x32x16_bf16 v[68:83], v[166:169], v[122:125], v[68:83]
	v_cvt_pk_bf16_f32 v118, v94, v95
	v_cvt_pk_bf16_f32 v119, v96, v97
	ds_read_b64_tr_b16 v[86:87], v255 offset:31744
	ds_read_b64_tr_b16 v[88:89], v255 offset:32256
	v_mfma_f32_32x32x16_bf16 v[52:67], v[154:157], v[122:125], v[52:67]
	v_cvt_pk_bf16_f32 v120, v98, v99
	v_cvt_pk_bf16_f32 v121, v100, v101
	v_lshlrev_b32_sdwa v248, s32, v225 dst_sel:DWORD dst_unused:UNUSED_PAD src0_sel:DWORD src1_sel:BYTE_0
	v_lshrrev_b32_sdwa v249, s11, v226 dst_sel:DWORD dst_unused:UNUSED_PAD src0_sel:DWORD src1_sel:BYTE_0
	ds_read_b64 v[114:115], v248 offset:51200
	ds_read_b64 v[116:117], v249 offset:51200
	v_max_f32_e32 v95, v69, v69
	v_max_f32_e32 v96, v68, v68
	v_max_f32_e32 v95, v96, v95
	s_nop 3
	v_max3_f32 v96, v70, v71, v53
	v_max3_f32 v95, v95, v52, v54
	v_max3_f32 v95, v95, v55, v72
	v_max3_f32 v96, v96, v74, v75
	v_max3_f32 v95, v95, v73, v56
	v_max3_f32 v96, v96, v58, v59
	v_max3_f32 v95, v95, v57, v76
	v_max3_f32 v96, v96, v78, v79
	v_max3_f32 v95, v95, v77, v60
	v_max3_f32 v96, v96, v62, v63
	v_max3_f32 v95, v95, v61, v80
	v_max3_f32 v96, v96, v82, v83
	v_max3_f32 v95, v95, v81, v64
	v_max3_f32 v96, v96, v66, v67
	v_max3_f32 v94, v95, v65, v96
	v_mov_b32_e32 v95, v94
	s_nop 1
	v_permlane32_swap_b32_e32 v94, v95
	v_max_f32_e32 v95, v95, v95
	v_max_f32_e32 v94, v94, v94
	v_max_f32_e32 v94, v94, v95
	v_cmp_lt_f32_e32 vcc, s14, v94
	s_cmp_lg_u64 vcc, 0
	s_cselect_b64 s[42:43], -1, 0
	s_cbranch_vccnz .LBB0_1284
; #define WAIT_BAR(N) asm volatile("s_waitcnt vmcnt(" #N ") lgkmcnt(0)\n\ts_barrier":::"memory")
;   #define RESC() do{ if(resc){ asm volatile("s_waitcnt lgkmcnt(0)":::"memory"); \
;       _Pragma("unroll") for(int d_=0;d_<2;++d_) _Pragma("unroll") for(int r=0;r<16;++r)o[d_][r]*=wsf[crow(r,hi)]; } }while(0)
;   #define ROT() do{sl_prev=sl_cur;sl_cur=sl_next;sl_next=(sl_next==(NSLOT-1)*SLOTB)?0:sl_next+SLOTB;}while(0)
; template<int THRL> __device__ __forceinline__ void attn_unit(int b,int h,int qb,const bf16*Q,const bf16*__restrict__ K,const bf16*__restrict__ V,bf16*O,const unsigned*MASK,char*shm){
;     ...
;   int t=1;
;   for(;t+5<NT;t+=2){
;     STEP(pB0,pB1,pA0,pA1,t,true,true,true,wB,wA);     WAIT_BAR(2); RESC(); ROT();
.LBB0_1277:
	s_waitcnt lgkmcnt(0)
	v_and_b32_e32 v146, v146, v114
	v_and_b32_e32 v147, v147, v115
	v_and_b32_e32 v148, v148, v116
	v_and_b32_e32 v149, v149, v117
	v_lshlrev_b32_sdwa v248, s32, v225 dst_sel:DWORD dst_unused:UNUSED_PAD src0_sel:DWORD src1_sel:BYTE_1
	v_lshrrev_b32_sdwa v249, s11, v226 dst_sel:DWORD dst_unused:UNUSED_PAD src0_sel:DWORD src1_sel:BYTE_1
	ds_read_b64 v[114:115], v248 offset:51200
	ds_read_b64 v[116:117], v249 offset:51200
	s_waitcnt lgkmcnt(14)
	v_mfma_f32_32x32x16_bf16 v[20:35], v[146:149], v[182:185], v[20:35]
	v_exp_f32_e32 v68, v68
	v_exp_f32_e32 v69, v69
	v_exp_f32_e32 v70, v70
	v_exp_f32_e32 v71, v71
	s_waitcnt lgkmcnt(12)
	v_mfma_f32_32x32x16_bf16 v[4:19], v[146:149], v[178:181], v[4:19]
	v_mfma_f32_32x32x16_bf16 v[228:243], v[146:149], v[204:207], v[228:243]
	v_exp_f32_e32 v72, v72
	v_exp_f32_e32 v73, v73
	v_exp_f32_e32 v74, v74
	v_exp_f32_e32 v75, v75
	s_waitcnt lgkmcnt(0)
	v_and_b32_e32 v142, v142, v114
	v_and_b32_e32 v143, v143, v115
	v_and_b32_e32 v144, v144, v116
	v_and_b32_e32 v145, v145, v117
	v_lshlrev_b32_sdwa v248, s32, v225 dst_sel:DWORD dst_unused:UNUSED_PAD src0_sel:DWORD src1_sel:BYTE_2
	v_lshrrev_b32_sdwa v249, s11, v226 dst_sel:DWORD dst_unused:UNUSED_PAD src0_sel:DWORD src1_sel:BYTE_2
	ds_read_b64 v[114:115], v248 offset:51200
	ds_read_b64 v[116:117], v249 offset:51200
	v_add_u32_e32 v94, s60, v221
	ds_read_b128 v[178:181], v94
	ds_read_b128 v[170:173], v94 offset:512
	s_waitcnt lgkmcnt(12)
	v_mfma_f32_32x32x16_bf16 v[20:35], v[142:145], v[150:153], v[20:35]
	v_exp_f32_e32 v76, v76
	v_exp_f32_e32 v77, v77
	v_exp_f32_e32 v78, v78
	v_exp_f32_e32 v79, v79
	ds_read_b128 v[174:177], v94 offset:2048
	ds_read_b128 v[162:165], v94 offset:2560
	s_waitcnt lgkmcnt(12)
	v_mfma_f32_32x32x16_bf16 v[4:19], v[142:145], v[110:113], v[4:19]
	v_mfma_f32_32x32x16_bf16 v[228:243], v[142:145], v[204:207], v[228:243]
	v_exp_f32_e32 v80, v80
	v_exp_f32_e32 v81, v81
	v_exp_f32_e32 v82, v82
	v_exp_f32_e32 v83, v83
	s_waitcnt lgkmcnt(4)
	v_and_b32_e32 v130, v130, v114
	v_and_b32_e32 v131, v131, v115
	v_and_b32_e32 v132, v132, v116
	v_and_b32_e32 v133, v133, v117
	v_lshlrev_b32_sdwa v248, s32, v225 dst_sel:DWORD dst_unused:UNUSED_PAD src0_sel:DWORD src1_sel:BYTE_3
	v_lshrrev_b32_sdwa v249, s11, v226 dst_sel:DWORD dst_unused:UNUSED_PAD src0_sel:DWORD src1_sel:BYTE_3
	ds_read_b64 v[114:115], v248 offset:51200
	ds_read_b64 v[116:117], v249 offset:51200
	ds_read_b128 v[166:169], v94 offset:4096
	ds_read_b128 v[154:157], v94 offset:4608
	s_waitcnt lgkmcnt(12)
	v_mfma_f32_32x32x16_bf16 v[20:35], v[130:133], v[106:109], v[20:35]
	v_exp_f32_e32 v52, v52
	v_exp_f32_e32 v53, v53
	v_exp_f32_e32 v54, v54
	v_exp_f32_e32 v55, v55
	ds_read_b128 v[158:161], v94 offset:6144
	ds_read_b128 v[150:153], v94 offset:6656
	s_waitcnt lgkmcnt(12)
	v_mfma_f32_32x32x16_bf16 v[4:19], v[130:133], v[102:105], v[4:19]
	v_mfma_f32_32x32x16_bf16 v[228:243], v[130:133], v[204:207], v[228:243]
	v_exp_f32_e32 v56, v56
	v_exp_f32_e32 v57, v57
	v_exp_f32_e32 v58, v58
	v_exp_f32_e32 v59, v59
	s_waitcnt lgkmcnt(4)
	v_and_b32_e32 v118, v118, v114
	v_and_b32_e32 v119, v119, v115
	v_and_b32_e32 v120, v120, v116
	v_and_b32_e32 v121, v121, v117
	s_nop 0
	s_waitcnt lgkmcnt(10)
	v_mfma_f32_32x32x16_bf16 v[20:35], v[118:121], v[90:93], v[20:35]
	v_exp_f32_e32 v60, v60
	v_exp_f32_e32 v61, v61
	v_exp_f32_e32 v62, v62
	v_exp_f32_e32 v63, v63
	s_waitcnt lgkmcnt(8)
	v_mfma_f32_32x32x16_bf16 v[4:19], v[118:121], v[86:89], v[4:19]
	v_mfma_f32_32x32x16_bf16 v[228:243], v[118:121], v[204:207], v[228:243]
	v_exp_f32_e32 v64, v64
	v_exp_f32_e32 v65, v65
	v_exp_f32_e32 v66, v66
	v_exp_f32_e32 v67, v67
	s_waitcnt vmcnt(3)
	v_and_b32_e32 v225, 0x0f0f0f0f, v2
	v_and_b32_e32 v226, 0xf0f0f0f0, v2
	s_waitcnt vmcnt(3) lgkmcnt(0)
	s_barrier
	s_andn2_b64 vcc, exec, s[42:43]
	s_cbranch_vccnz .LBB0_1279
	s_waitcnt lgkmcnt(0)
	ds_read_b128 v[86:89], v85 offset:49248
	ds_read_b128 v[90:93], v85 offset:49216
	ds_read_b128 v[94:97], v85 offset:49184
	ds_read_b128 v[98:101], v85 offset:49152
	s_waitcnt lgkmcnt(3)
	v_pk_mul_f32 v[32:33], v[32:33], v[86:87]
	s_waitcnt lgkmcnt(2)
	v_pk_mul_f32 v[28:29], v[28:29], v[90:91]
	s_waitcnt lgkmcnt(1)
	v_pk_mul_f32 v[24:25], v[24:25], v[94:95]
	v_pk_mul_f32 v[34:35], v[34:35], v[88:89]
	v_pk_mul_f32 v[30:31], v[30:31], v[92:93]
	v_pk_mul_f32 v[26:27], v[26:27], v[96:97]
	s_waitcnt lgkmcnt(0)
	v_pk_mul_f32 v[22:23], v[22:23], v[100:101]
	v_pk_mul_f32 v[20:21], v[20:21], v[98:99]
	v_pk_mul_f32 v[16:17], v[16:17], v[86:87]
	v_pk_mul_f32 v[12:13], v[12:13], v[90:91]
	v_pk_mul_f32 v[8:9], v[8:9], v[94:95]
	v_pk_mul_f32 v[18:19], v[18:19], v[88:89]
	v_pk_mul_f32 v[14:15], v[14:15], v[92:93]
	v_pk_mul_f32 v[10:11], v[10:11], v[96:97]
	v_pk_mul_f32 v[6:7], v[6:7], v[100:101]
	v_pk_mul_f32 v[4:5], v[4:5], v[98:99]
	v_pk_mul_f32 v[240:241], v[240:241], v[86:87]
	v_pk_mul_f32 v[236:237], v[236:237], v[90:91]
	v_pk_mul_f32 v[232:233], v[232:233], v[94:95]
	v_pk_mul_f32 v[242:243], v[242:243], v[88:89]
	v_pk_mul_f32 v[238:239], v[238:239], v[92:93]
	v_pk_mul_f32 v[234:235], v[234:235], v[96:97]
	v_pk_mul_f32 v[230:231], v[230:231], v[100:101]
	v_pk_mul_f32 v[228:229], v[228:229], v[98:99]

;   #define RESC() do{ if(resc){ asm volatile("s_waitcnt lgkmcnt(0)":::"memory"); \
;       _Pragma("unroll") for(int d_=0;d_<2;++d_) _Pragma("unroll") for(int r=0;r<16;++r)o[d_][r]*=wsf[crow(r,hi)]; } }while(0)
;   #define ROT() do{sl_prev=sl_cur;sl_cur=sl_next;sl_next=(sl_next==(NSLOT-1)*SLOTB)?0:sl_next+SLOTB;}while(0)
;   #define ENDW(tt) do{ if((tt)+3<NT){WAIT_BAR(2);} else if((tt)+2<NT){WAIT_BAR(1);} else {WAIT_BAR(0);} }while(0)
; template<int THRL> __device__ __forceinline__ void attn_unit(int b,int h,int qb,const bf16*Q,const bf16*__restrict__ K,const bf16*__restrict__ V,bf16*O,const unsigned*MASK,char*shm){
;     ...
;   for(;t+1<NT;t+=2){
;     STEP(pB0,pB1,pA0,pA1,t,(t+3<NT),(t+1<NT),(t+1<NT),wB,wA);       ENDW(t);   RESC(); ROT();
;     STEP(pA0,pA1,pB0,pB1,t+1,(t+4<NT),(t+2<NT),(t+2<NT),wA,wB);     ENDW(t+1); RESC(); ROT();
.LBB0_1290:
	global_load_dword v223, v[210:211], off
	v_add_u32_e32 v85, s48, v220
	ds_read_b64_tr_b16 v[186:187], v85 offset:24576
	ds_read_b64_tr_b16 v[188:189], v85 offset:25088
	s_waitcnt lgkmcnt(9)
	v_mfma_f32_32x32x16_bf16 v[102:117], v[178:181], v[138:141], v[36:51]
	v_cvt_pk_bf16_f32 v146, v68, v69
	v_cvt_pk_bf16_f32 v147, v70, v71
	ds_read_b64_tr_b16 v[178:179], v85 offset:28672
	ds_read_b64_tr_b16 v[180:181], v85 offset:29184
	s_waitcnt lgkmcnt(10)
	v_mfma_f32_32x32x16_bf16 v[86:101], v[170:173], v[138:141], v[36:51]
	v_cvt_pk_bf16_f32 v148, v72, v73
	v_cvt_pk_bf16_f32 v149, v74, v75
	ds_read_b64_tr_b16 v[182:183], v85 offset:25600
	ds_read_b64_tr_b16 v[184:185], v85 offset:26112
	s_waitcnt lgkmcnt(11)
	v_mfma_f32_32x32x16_bf16 v[102:117], v[174:177], v[134:137], v[102:117]
	v_cvt_pk_bf16_f32 v142, v76, v77
	v_cvt_pk_bf16_f32 v143, v78, v79
	ds_read_b64_tr_b16 v[76:77], v85 offset:29696
	ds_read_b64_tr_b16 v[78:79], v85 offset:30208
	s_waitcnt lgkmcnt(12)
	v_mfma_f32_32x32x16_bf16 v[86:101], v[162:165], v[134:137], v[86:101]
	v_cvt_pk_bf16_f32 v144, v80, v81
	v_cvt_pk_bf16_f32 v145, v82, v83
	ds_read_b64_tr_b16 v[72:73], v85 offset:26624
	ds_read_b64_tr_b16 v[74:75], v85 offset:27136
	s_waitcnt lgkmcnt(13)
	v_mfma_f32_32x32x16_bf16 v[102:117], v[166:169], v[126:129], v[102:117]
	v_cvt_pk_bf16_f32 v130, v52, v53
	v_cvt_pk_bf16_f32 v131, v54, v55
	ds_read_b64_tr_b16 v[68:69], v85 offset:30720
	ds_read_b64_tr_b16 v[70:71], v85 offset:31232
	s_waitcnt lgkmcnt(14)
	v_mfma_f32_32x32x16_bf16 v[86:101], v[154:157], v[126:129], v[86:101]
	v_cvt_pk_bf16_f32 v132, v56, v57
	v_cvt_pk_bf16_f32 v133, v58, v59
	ds_read_b64_tr_b16 v[56:57], v85 offset:27648
	ds_read_b64_tr_b16 v[58:59], v85 offset:28160
	s_waitcnt lgkmcnt(14)
	v_mfma_f32_32x32x16_bf16 v[102:117], v[158:161], v[122:125], v[102:117]
	v_cvt_pk_bf16_f32 v118, v60, v61
	v_cvt_pk_bf16_f32 v119, v62, v63
	ds_read_b64_tr_b16 v[52:53], v85 offset:31744
	ds_read_b64_tr_b16 v[54:55], v85 offset:32256
	v_mfma_f32_32x32x16_bf16 v[86:101], v[150:153], v[122:125], v[86:101]
	v_cvt_pk_bf16_f32 v120, v64, v65
	v_cvt_pk_bf16_f32 v121, v66, v67
	v_lshlrev_b32_sdwa v248, s32, v225 dst_sel:DWORD dst_unused:UNUSED_PAD src0_sel:DWORD src1_sel:BYTE_0
	v_lshrrev_b32_sdwa v249, s11, v226 dst_sel:DWORD dst_unused:UNUSED_PAD src0_sel:DWORD src1_sel:BYTE_0
	ds_read_b64 v[80:81], v248 offset:51200
	ds_read_b64 v[82:83], v249 offset:51200
	s_add_i32 s65, s64, -1
	s_cmp_ge_i32 s65, s61
	s_cselect_b64 s[48:49], -1, 0
	s_and_b64 vcc, exec, s[48:49]
	s_cbranch_vccnz .LBB0_1292
	v_lshl_add_u64 v[62:63], v[194:195], 0, s[46:47]
	s_add_i32 s4, s60, s58
	v_lshl_add_u64 v[62:63], v[62:63], 0, s[82:83]
	s_mov_b32 s5, m0
	s_mov_b32 m0, s4
	s_nop 0
	global_load_lds_dwordx4 v[62:63], off
	s_mov_b32 m0, s5

; #define WAIT_BAR(N) asm volatile("s_waitcnt vmcnt(" #N ") lgkmcnt(0)\n\ts_barrier":::"memory")
;   #define RESC() do{ if(resc){ asm volatile("s_waitcnt lgkmcnt(0)":::"memory"); \
;       _Pragma("unroll") for(int d_=0;d_<2;++d_) _Pragma("unroll") for(int r=0;r<16;++r)o[d_][r]*=wsf[crow(r,hi)]; } }while(0)
;   #define ROT() do{sl_prev=sl_cur;sl_cur=sl_next;sl_next=(sl_next==(NSLOT-1)*SLOTB)?0:sl_next+SLOTB;}while(0)
;   #define ENDW(tt) do{ if((tt)+3<NT){WAIT_BAR(2);} else if((tt)+2<NT){WAIT_BAR(1);} else {WAIT_BAR(0);} }while(0)
; template<int THRL> __device__ __forceinline__ void attn_unit(int b,int h,int qb,const bf16*Q,const bf16*__restrict__ K,const bf16*__restrict__ V,bf16*O,const unsigned*MASK,char*shm){
;     ...
;   int t=1;
;   for(;t+5<NT;t+=2){
;     STEP(pB0,pB1,pA0,pA1,t,true,true,true,wB,wA);     WAIT_BAR(2); RESC(); ROT();
;     STEP(pA0,pA1,pB0,pB1,t+1,true,true,true,wA,wB);   WAIT_BAR(2); RESC(); ROT();
;   }
;     ...
;   for(;t+1<NT;t+=2){
;     STEP(pB0,pB1,pA0,pA1,t,(t+3<NT),(t+1<NT),(t+1<NT),wB,wA);       ENDW(t);   RESC(); ROT();
;     STEP(pA0,pA1,pB0,pB1,t+1,(t+4<NT),(t+2<NT),(t+2<NT),wA,wB);     ENDW(t+1); RESC(); ROT();
.LBB0_1293:
	s_waitcnt lgkmcnt(0)
	v_and_b32_e32 v146, v146, v80
	v_and_b32_e32 v147, v147, v81
	v_and_b32_e32 v148, v148, v82
	v_and_b32_e32 v149, v149, v83
	v_lshlrev_b32_sdwa v248, s32, v225 dst_sel:DWORD dst_unused:UNUSED_PAD src0_sel:DWORD src1_sel:BYTE_1
	v_lshrrev_b32_sdwa v249, s11, v226 dst_sel:DWORD dst_unused:UNUSED_PAD src0_sel:DWORD src1_sel:BYTE_1
	ds_read_b64 v[80:81], v248 offset:51200
	ds_read_b64 v[82:83], v249 offset:51200
	s_waitcnt lgkmcnt(14)
	v_mfma_f32_32x32x16_bf16 v[20:35], v[146:149], v[186:189], v[20:35]
	v_exp_f32_e32 v102, v102
	v_exp_f32_e32 v103, v103
	v_exp_f32_e32 v104, v104
	v_exp_f32_e32 v105, v105
	s_waitcnt lgkmcnt(12)
	v_mfma_f32_32x32x16_bf16 v[4:19], v[146:149], v[178:181], v[4:19]
	v_mfma_f32_32x32x16_bf16 v[228:243], v[146:149], v[204:207], v[228:243]
	v_exp_f32_e32 v106, v106
	v_exp_f32_e32 v107, v107
	v_exp_f32_e32 v108, v108
	v_exp_f32_e32 v109, v109
	s_waitcnt lgkmcnt(0)
	v_and_b32_e32 v142, v142, v80
	v_and_b32_e32 v143, v143, v81
	v_and_b32_e32 v144, v144, v82
	v_and_b32_e32 v145, v145, v83
	v_lshlrev_b32_sdwa v248, s32, v225 dst_sel:DWORD dst_unused:UNUSED_PAD src0_sel:DWORD src1_sel:BYTE_2
	v_lshrrev_b32_sdwa v249, s11, v226 dst_sel:DWORD dst_unused:UNUSED_PAD src0_sel:DWORD src1_sel:BYTE_2
	ds_read_b64 v[80:81], v248 offset:51200
	ds_read_b64 v[82:83], v249 offset:51200
	v_add_u32_e32 v60, s62, v221
	ds_read_b128 v[178:181], v60
	ds_read_b128 v[170:173], v60 offset:512
	s_waitcnt lgkmcnt(12)
	v_mfma_f32_32x32x16_bf16 v[20:35], v[142:145], v[182:185], v[20:35]
	v_exp_f32_e32 v110, v110
	v_exp_f32_e32 v111, v111
	v_exp_f32_e32 v112, v112
	v_exp_f32_e32 v113, v113
	ds_read_b128 v[174:177], v60 offset:2048
	ds_read_b128 v[162:165], v60 offset:2560
	s_waitcnt lgkmcnt(12)
	v_mfma_f32_32x32x16_bf16 v[4:19], v[142:145], v[76:79], v[4:19]
	v_mfma_f32_32x32x16_bf16 v[228:243], v[142:145], v[204:207], v[228:243]
	v_exp_f32_e32 v114, v114
	v_exp_f32_e32 v115, v115
	v_exp_f32_e32 v116, v116
	v_exp_f32_e32 v117, v117
	s_waitcnt lgkmcnt(4)
	v_and_b32_e32 v130, v130, v80
	v_and_b32_e32 v131, v131, v81
	v_and_b32_e32 v132, v132, v82
	v_and_b32_e32 v133, v133, v83
	v_lshlrev_b32_sdwa v248, s32, v225 dst_sel:DWORD dst_unused:UNUSED_PAD src0_sel:DWORD src1_sel:BYTE_3
	v_lshrrev_b32_sdwa v249, s11, v226 dst_sel:DWORD dst_unused:UNUSED_PAD src0_sel:DWORD src1_sel:BYTE_3
	ds_read_b64 v[80:81], v248 offset:51200
	ds_read_b64 v[82:83], v249 offset:51200
	ds_read_b128 v[166:169], v60 offset:4096
	ds_read_b128 v[154:157], v60 offset:4608
	s_waitcnt lgkmcnt(12)
	v_mfma_f32_32x32x16_bf16 v[20:35], v[130:133], v[72:75], v[20:35]
	v_exp_f32_e32 v86, v86
	v_exp_f32_e32 v87, v87
	v_exp_f32_e32 v88, v88
	v_exp_f32_e32 v89, v89
	ds_read_b128 v[158:161], v60 offset:6144
	ds_read_b128 v[150:153], v60 offset:6656
	s_waitcnt lgkmcnt(12)
	v_mfma_f32_32x32x16_bf16 v[4:19], v[130:133], v[68:71], v[4:19]
	v_mfma_f32_32x32x16_bf16 v[228:243], v[130:133], v[204:207], v[228:243]
	v_exp_f32_e32 v90, v90
	v_exp_f32_e32 v91, v91
	v_exp_f32_e32 v92, v92
	v_exp_f32_e32 v93, v93
	s_waitcnt lgkmcnt(4)
	v_and_b32_e32 v118, v118, v80
	v_and_b32_e32 v119, v119, v81
	v_and_b32_e32 v120, v120, v82
	v_and_b32_e32 v121, v121, v83
	s_nop 0
	s_waitcnt lgkmcnt(10)
	v_mfma_f32_32x32x16_bf16 v[20:35], v[118:121], v[56:59], v[20:35]
	v_exp_f32_e32 v94, v94
	v_exp_f32_e32 v95, v95
	v_exp_f32_e32 v96, v96
	v_exp_f32_e32 v97, v97
	s_waitcnt lgkmcnt(8)
	v_mfma_f32_32x32x16_bf16 v[4:19], v[118:121], v[52:55], v[4:19]
	v_mfma_f32_32x32x16_bf16 v[228:243], v[118:121], v[204:207], v[228:243]
	v_exp_f32_e32 v98, v98
	v_exp_f32_e32 v99, v99
	v_exp_f32_e32 v100, v100
	v_exp_f32_e32 v101, v101
	v_and_b32_e32 v225, 0x0f0f0f0f, v218
	v_and_b32_e32 v226, 0xf0f0f0f0, v218
	s_mov_b64 s[4:5], -1
	s_and_b64 vcc, exec, s[48:49]
	s_cbranch_vccnz .LBB0_1318
	s_andn2_b64 vcc, exec, s[4:5]
	s_cbranch_vccz .LBB0_1323

;   #define RESC() do{ if(resc){ asm volatile("s_waitcnt lgkmcnt(0)":::"memory"); \
;       _Pragma("unroll") for(int d_=0;d_<2;++d_) _Pragma("unroll") for(int r=0;r<16;++r)o[d_][r]*=wsf[crow(r,hi)]; } }while(0)
;   #define ROT() do{sl_prev=sl_cur;sl_cur=sl_next;sl_next=(sl_next==(NSLOT-1)*SLOTB)?0:sl_next+SLOTB;}while(0)
;   #define ENDW(tt) do{ if((tt)+3<NT){WAIT_BAR(2);} else if((tt)+2<NT){WAIT_BAR(1);} else {WAIT_BAR(0);} }while(0)
; template<int THRL> __device__ __forceinline__ void attn_unit(int b,int h,int qb,const bf16*Q,const bf16*__restrict__ K,const bf16*__restrict__ V,bf16*O,const unsigned*MASK,char*shm){
;     ...
;   for(;t+1<NT;t+=2){
;     STEP(pB0,pB1,pA0,pA1,t,(t+3<NT),(t+1<NT),(t+1<NT),wB,wA);       ENDW(t);   RESC(); ROT();
;     STEP(pA0,pA1,pB0,pB1,t+1,(t+4<NT),(t+2<NT),(t+2<NT),wA,wB);     ENDW(t+1); RESC(); ROT();
.LBB0_1299:
	v_add_u32_e32 v255, s60, v220
	ds_read_b64_tr_b16 v[190:191], v255 offset:24576
	ds_read_b64_tr_b16 v[192:193], v255 offset:25088
	s_waitcnt lgkmcnt(9)
	v_mfma_f32_32x32x16_bf16 v[68:83], v[178:181], v[138:141], v[36:51]
	v_cvt_pk_bf16_f32 v146, v102, v103
	v_cvt_pk_bf16_f32 v147, v104, v105
	ds_read_b64_tr_b16 v[186:187], v255 offset:28672
	ds_read_b64_tr_b16 v[188:189], v255 offset:29184
	s_waitcnt lgkmcnt(10)
	v_mfma_f32_32x32x16_bf16 v[52:67], v[170:173], v[138:141], v[36:51]
	v_cvt_pk_bf16_f32 v148, v106, v107
	v_cvt_pk_bf16_f32 v149, v108, v109
	ds_read_b64_tr_b16 v[182:183], v255 offset:25600
	ds_read_b64_tr_b16 v[184:185], v255 offset:26112
	s_waitcnt lgkmcnt(11)
	v_mfma_f32_32x32x16_bf16 v[68:83], v[174:177], v[134:137], v[68:83]
	v_cvt_pk_bf16_f32 v142, v110, v111
	v_cvt_pk_bf16_f32 v143, v112, v113
	ds_read_b64_tr_b16 v[110:111], v255 offset:29696
	ds_read_b64_tr_b16 v[112:113], v255 offset:30208
	s_waitcnt lgkmcnt(12)
	v_mfma_f32_32x32x16_bf16 v[52:67], v[162:165], v[134:137], v[52:67]
	v_cvt_pk_bf16_f32 v144, v114, v115
	v_cvt_pk_bf16_f32 v145, v116, v117
	ds_read_b64_tr_b16 v[106:107], v255 offset:26624
	ds_read_b64_tr_b16 v[108:109], v255 offset:27136
	s_waitcnt lgkmcnt(13)
	v_mfma_f32_32x32x16_bf16 v[68:83], v[166:169], v[126:129], v[68:83]
	v_cvt_pk_bf16_f32 v130, v86, v87
	v_cvt_pk_bf16_f32 v131, v88, v89
	ds_read_b64_tr_b16 v[102:103], v255 offset:30720
	ds_read_b64_tr_b16 v[104:105], v255 offset:31232
	s_waitcnt lgkmcnt(14)
	v_mfma_f32_32x32x16_bf16 v[52:67], v[154:157], v[126:129], v[52:67]
	v_cvt_pk_bf16_f32 v132, v90, v91
	v_cvt_pk_bf16_f32 v133, v92, v93
	ds_read_b64_tr_b16 v[90:91], v255 offset:27648
	ds_read_b64_tr_b16 v[92:93], v255 offset:28160
	s_waitcnt lgkmcnt(14)
	v_mfma_f32_32x32x16_bf16 v[68:83], v[158:161], v[122:125], v[68:83]
	v_cvt_pk_bf16_f32 v118, v94, v95
	v_cvt_pk_bf16_f32 v119, v96, v97
	ds_read_b64_tr_b16 v[86:87], v255 offset:31744
	ds_read_b64_tr_b16 v[88:89], v255 offset:32256
	v_mfma_f32_32x32x16_bf16 v[52:67], v[150:153], v[122:125], v[52:67]
	v_cvt_pk_bf16_f32 v120, v98, v99
	v_cvt_pk_bf16_f32 v121, v100, v101
	v_lshlrev_b32_sdwa v248, s32, v225 dst_sel:DWORD dst_unused:UNUSED_PAD src0_sel:DWORD src1_sel:BYTE_0
	v_lshrrev_b32_sdwa v249, s11, v226 dst_sel:DWORD dst_unused:UNUSED_PAD src0_sel:DWORD src1_sel:BYTE_0
	ds_read_b64 v[114:115], v248 offset:51200
	ds_read_b64 v[116:117], v249 offset:51200
	s_cmp_ge_i32 s64, s61
	s_cselect_b64 s[50:51], -1, 0
	s_and_b64 vcc, exec, s[50:51]
	s_cbranch_vccnz .LBB0_1301
	v_lshl_add_u64 v[96:97], v[194:195], 0, s[46:47]
	s_mov_b64 s[4:5], 0x40000
	s_add_i32 s42, s62, s58
	v_lshl_add_u64 v[96:97], v[96:97], 0, s[4:5]
	s_mov_b32 s4, m0
	s_mov_b32 m0, s42
	s_nop 0
	global_load_lds_dwordx4 v[96:97], off
	s_mov_b32 m0, s4

.LBB0_1304:
	s_waitcnt lgkmcnt(0)
	v_and_b32_e32 v146, v146, v114
	v_and_b32_e32 v147, v147, v115
	v_and_b32_e32 v148, v148, v116
	v_and_b32_e32 v149, v149, v117
	v_lshlrev_b32_sdwa v248, s32, v225 dst_sel:DWORD dst_unused:UNUSED_PAD src0_sel:DWORD src1_sel:BYTE_1
	v_lshrrev_b32_sdwa v249, s11, v226 dst_sel:DWORD dst_unused:UNUSED_PAD src0_sel:DWORD src1_sel:BYTE_1
	ds_read_b64 v[114:115], v248 offset:51200
	ds_read_b64 v[116:117], v249 offset:51200
	s_waitcnt lgkmcnt(14)
	v_mfma_f32_32x32x16_bf16 v[20:35], v[146:149], v[190:193], v[20:35]
	v_exp_f32_e32 v68, v68
	v_exp_f32_e32 v69, v69
	v_exp_f32_e32 v70, v70
	v_exp_f32_e32 v71, v71
	s_waitcnt lgkmcnt(12)
	v_mfma_f32_32x32x16_bf16 v[4:19], v[146:149], v[186:189], v[4:19]
	v_mfma_f32_32x32x16_bf16 v[228:243], v[146:149], v[204:207], v[228:243]
	v_exp_f32_e32 v72, v72
	v_exp_f32_e32 v73, v73
	v_exp_f32_e32 v74, v74
	v_exp_f32_e32 v75, v75
	s_waitcnt lgkmcnt(0)
	v_and_b32_e32 v142, v142, v114
	v_and_b32_e32 v143, v143, v115
	v_and_b32_e32 v144, v144, v116
	v_and_b32_e32 v145, v145, v117
	v_lshlrev_b32_sdwa v248, s32, v225 dst_sel:DWORD dst_unused:UNUSED_PAD src0_sel:DWORD src1_sel:BYTE_2
	v_lshrrev_b32_sdwa v249, s11, v226 dst_sel:DWORD dst_unused:UNUSED_PAD src0_sel:DWORD src1_sel:BYTE_2
	ds_read_b64 v[114:115], v248 offset:51200
	ds_read_b64 v[116:117], v249 offset:51200
	s_and_b64 vcc, exec, s[42:43]
	s_cbranch_vccnz .LBB0_1306
	v_add_u32_e32 v85, s60, v221
	ds_read_b128 v[178:181], v85
	ds_read_b128 v[170:173], v85 offset:512

.LBB0_1308:
	s_waitcnt lgkmcnt(8)
	v_mfma_f32_32x32x16_bf16 v[4:19], v[142:145], v[110:113], v[4:19]
	v_mfma_f32_32x32x16_bf16 v[228:243], v[142:145], v[204:207], v[228:243]
	v_exp_f32_e32 v80, v80
	v_exp_f32_e32 v81, v81
	v_exp_f32_e32 v82, v82
	v_exp_f32_e32 v83, v83
	s_waitcnt lgkmcnt(0)
	v_and_b32_e32 v130, v130, v114
	v_and_b32_e32 v131, v131, v115
	v_and_b32_e32 v132, v132, v116
	v_and_b32_e32 v133, v133, v117
	v_lshlrev_b32_sdwa v248, s32, v225 dst_sel:DWORD dst_unused:UNUSED_PAD src0_sel:DWORD src1_sel:BYTE_3
	v_lshrrev_b32_sdwa v249, s11, v226 dst_sel:DWORD dst_unused:UNUSED_PAD src0_sel:DWORD src1_sel:BYTE_3
	ds_read_b64 v[114:115], v248 offset:51200
	ds_read_b64 v[116:117], v249 offset:51200
	s_and_b64 vcc, exec, s[42:43]
	s_cbranch_vccnz .LBB0_1310
	v_add_u32_e32 v85, s60, v221
	ds_read_b128 v[166:169], v85 offset:4096
	ds_read_b128 v[154:157], v85 offset:4608

; #define WAIT_BAR(N) asm volatile("s_waitcnt vmcnt(" #N ") lgkmcnt(0)\n\ts_barrier":::"memory")
;   #define RESC() do{ if(resc){ asm volatile("s_waitcnt lgkmcnt(0)":::"memory"); \
;       _Pragma("unroll") for(int d_=0;d_<2;++d_) _Pragma("unroll") for(int r=0;r<16;++r)o[d_][r]*=wsf[crow(r,hi)]; } }while(0)
;   #define ROT() do{sl_prev=sl_cur;sl_cur=sl_next;sl_next=(sl_next==(NSLOT-1)*SLOTB)?0:sl_next+SLOTB;}while(0)
;   #define ENDW(tt) do{ if((tt)+3<NT){WAIT_BAR(2);} else if((tt)+2<NT){WAIT_BAR(1);} else {WAIT_BAR(0);} }while(0)
; template<int THRL> __device__ __forceinline__ void attn_unit(int b,int h,int qb,const bf16*Q,const bf16*__restrict__ K,const bf16*__restrict__ V,bf16*O,const unsigned*MASK,char*shm){
;     ...
;   int t=1;
;   for(;t+5<NT;t+=2){
;     STEP(pB0,pB1,pA0,pA1,t,true,true,true,wB,wA);     WAIT_BAR(2); RESC(); ROT();
;     STEP(pA0,pA1,pB0,pB1,t+1,true,true,true,wA,wB);   WAIT_BAR(2); RESC(); ROT();
;   }
;     ...
;   for(;t+1<NT;t+=2){
;     STEP(pB0,pB1,pA0,pA1,t,(t+3<NT),(t+1<NT),(t+1<NT),wB,wA);       ENDW(t);   RESC(); ROT();
;     STEP(pA0,pA1,pB0,pB1,t+1,(t+4<NT),(t+2<NT),(t+2<NT),wA,wB);     ENDW(t+1); RESC(); ROT();
.LBB0_1312:
	s_waitcnt lgkmcnt(4)
	v_mfma_f32_32x32x16_bf16 v[4:19], v[130:133], v[102:105], v[4:19]
	v_mfma_f32_32x32x16_bf16 v[228:243], v[130:133], v[204:207], v[228:243]
	v_exp_f32_e32 v56, v56
	v_exp_f32_e32 v57, v57
	v_exp_f32_e32 v58, v58
	v_exp_f32_e32 v59, v59
	s_waitcnt lgkmcnt(0)
	v_and_b32_e32 v118, v118, v114
	v_and_b32_e32 v119, v119, v115
	v_and_b32_e32 v120, v120, v116
	v_and_b32_e32 v121, v121, v117
	s_nop 0
	s_waitcnt lgkmcnt(2)
	v_mfma_f32_32x32x16_bf16 v[20:35], v[118:121], v[90:93], v[20:35]
	v_exp_f32_e32 v60, v60
	v_exp_f32_e32 v61, v61
	v_exp_f32_e32 v62, v62
	v_exp_f32_e32 v63, v63
	s_waitcnt lgkmcnt(0)
	v_mfma_f32_32x32x16_bf16 v[4:19], v[118:121], v[86:89], v[4:19]
	v_mfma_f32_32x32x16_bf16 v[228:243], v[118:121], v[204:207], v[228:243]
	v_exp_f32_e32 v64, v64
	v_exp_f32_e32 v65, v65
	v_exp_f32_e32 v66, v66
	v_exp_f32_e32 v67, v67
	v_and_b32_e32 v225, 0x0f0f0f0f, v223
	v_and_b32_e32 v226, 0xf0f0f0f0, v223
	s_mov_b64 s[4:5], -1
	s_and_b64 vcc, exec, s[50:51]
	s_cbranch_vccnz .LBB0_1324
	s_andn2_b64 vcc, exec, s[4:5]
	s_cbranch_vccz .LBB0_1329

; #define WAIT_BAR(N) asm volatile("s_waitcnt vmcnt(" #N ") lgkmcnt(0)\n\ts_barrier":::"memory")
;   #define RESC() do{ if(resc){ asm volatile("s_waitcnt lgkmcnt(0)":::"memory"); \
;       _Pragma("unroll") for(int d_=0;d_<2;++d_) _Pragma("unroll") for(int r=0;r<16;++r)o[d_][r]*=wsf[crow(r,hi)]; } }while(0)
;   #define ROT() do{sl_prev=sl_cur;sl_cur=sl_next;sl_next=(sl_next==(NSLOT-1)*SLOTB)?0:sl_next+SLOTB;}while(0)
;   #define ENDW(tt) do{ if((tt)+3<NT){WAIT_BAR(2);} else if((tt)+2<NT){WAIT_BAR(1);} else {WAIT_BAR(0);} }while(0)
; template<int THRL> __device__ __forceinline__ void attn_unit(int b,int h,int qb,const bf16*Q,const bf16*__restrict__ K,const bf16*__restrict__ V,bf16*O,const unsigned*MASK,char*shm){
;     ...
;   int t=1;
;   for(;t+5<NT;t+=2){
;     STEP(pB0,pB1,pA0,pA1,t,true,true,true,wB,wA);     WAIT_BAR(2); RESC(); ROT();
;     STEP(pA0,pA1,pB0,pB1,t+1,true,true,true,wA,wB);   WAIT_BAR(2); RESC(); ROT();
;   }
;     ...
;   for(;t+1<NT;t+=2){
;     STEP(pB0,pB1,pA0,pA1,t,(t+3<NT),(t+1<NT),(t+1<NT),wB,wA);       ENDW(t);   RESC(); ROT();
;     STEP(pA0,pA1,pB0,pB1,t+1,(t+4<NT),(t+2<NT),(t+2<NT),wA,wB);     ENDW(t+1); RESC(); ROT();
;   }
;   STEP(pB0,pB1,pA0,pA1,NT-1,false,false,false,wB,wA); RESC();
.LBB0_1337:
	v_add_u32_e32 v2, s62, v220
	ds_read_b64_tr_b16 v[114:115], v2 offset:24576
	ds_read_b64_tr_b16 v[116:117], v2 offset:25088
	s_waitcnt lgkmcnt(9)
	v_mfma_f32_32x32x16_bf16 v[86:101], v[178:181], v[138:141], v[36:51]
	v_cvt_pk_bf16_f32 v146, v68, v69
	v_cvt_pk_bf16_f32 v147, v70, v71
	ds_read_b64_tr_b16 v[110:111], v2 offset:28672
	ds_read_b64_tr_b16 v[112:113], v2 offset:29184
	s_waitcnt lgkmcnt(10)
	v_mfma_f32_32x32x16_bf16 v[36:51], v[170:173], v[138:141], v[36:51]
	v_cvt_pk_bf16_f32 v148, v72, v73
	v_cvt_pk_bf16_f32 v149, v74, v75
	ds_read_b64_tr_b16 v[106:107], v2 offset:25600
	ds_read_b64_tr_b16 v[108:109], v2 offset:26112
	s_waitcnt lgkmcnt(11)
	v_mfma_f32_32x32x16_bf16 v[86:101], v[174:177], v[134:137], v[86:101]
	v_cvt_pk_bf16_f32 v142, v76, v77
	v_cvt_pk_bf16_f32 v143, v78, v79
	ds_read_b64_tr_b16 v[102:103], v2 offset:29696
	ds_read_b64_tr_b16 v[104:105], v2 offset:30208
	s_waitcnt lgkmcnt(12)
	v_mfma_f32_32x32x16_bf16 v[36:51], v[162:165], v[134:137], v[36:51]
	v_cvt_pk_bf16_f32 v144, v80, v81
	v_cvt_pk_bf16_f32 v145, v82, v83
	ds_read_b64_tr_b16 v[80:81], v2 offset:26624
	ds_read_b64_tr_b16 v[82:83], v2 offset:27136
	s_waitcnt lgkmcnt(13)
	v_mfma_f32_32x32x16_bf16 v[86:101], v[166:169], v[126:129], v[86:101]
	v_cvt_pk_bf16_f32 v130, v52, v53
	v_cvt_pk_bf16_f32 v131, v54, v55
	ds_read_b64_tr_b16 v[76:77], v2 offset:30720
	ds_read_b64_tr_b16 v[78:79], v2 offset:31232
	s_waitcnt lgkmcnt(14)
	v_mfma_f32_32x32x16_bf16 v[36:51], v[154:157], v[126:129], v[36:51]
	v_cvt_pk_bf16_f32 v132, v56, v57
	v_cvt_pk_bf16_f32 v133, v58, v59
	ds_read_b64_tr_b16 v[72:73], v2 offset:27648
	ds_read_b64_tr_b16 v[74:75], v2 offset:28160
	s_waitcnt lgkmcnt(14)
	v_mfma_f32_32x32x16_bf16 v[86:101], v[158:161], v[122:125], v[86:101]
	v_cvt_pk_bf16_f32 v118, v60, v61
	v_cvt_pk_bf16_f32 v119, v62, v63
	ds_read_b64_tr_b16 v[68:69], v2 offset:31744
	ds_read_b64_tr_b16 v[70:71], v2 offset:32256
	v_mfma_f32_32x32x16_bf16 v[36:51], v[150:153], v[122:125], v[36:51]
	v_cvt_pk_bf16_f32 v120, v64, v65
	v_cvt_pk_bf16_f32 v121, v66, v67
	v_lshlrev_b32_sdwa v248, s32, v225 dst_sel:DWORD dst_unused:UNUSED_PAD src0_sel:DWORD src1_sel:BYTE_0
	v_lshrrev_b32_sdwa v249, s11, v226 dst_sel:DWORD dst_unused:UNUSED_PAD src0_sel:DWORD src1_sel:BYTE_0
	ds_read_b64 v[154:155], v248 offset:51200
	ds_read_b64 v[156:157], v249 offset:51200
	v_max_f32_e32 v52, v87, v87
	v_max_f32_e32 v53, v86, v86
	v_max_f32_e32 v52, v53, v52
	s_nop 3
	v_max3_f32 v53, v88, v89, v37
	v_max3_f32 v52, v52, v36, v38
	v_max3_f32 v52, v52, v39, v90
	v_max3_f32 v53, v53, v92, v93
	v_max3_f32 v52, v52, v91, v40
	v_max3_f32 v53, v53, v42, v43
	v_max3_f32 v52, v52, v41, v94
	v_max3_f32 v53, v53, v96, v97
	v_max3_f32 v52, v52, v95, v44
	v_max3_f32 v53, v53, v46, v47
	v_max3_f32 v52, v52, v45, v98
	v_max3_f32 v53, v53, v100, v101
	v_max3_f32 v52, v52, v99, v48
	v_max3_f32 v53, v53, v50, v51
	v_max3_f32 v52, v52, v49, v53
	v_mov_b32_e32 v53, v52
	s_nop 1
	v_permlane32_swap_b32_e32 v52, v53
	v_max_f32_e32 v53, v53, v53
	v_max_f32_e32 v52, v52, v52
	v_max_f32_e32 v52, v52, v53
	v_cmp_lt_f32_e32 vcc, s14, v52
	s_cmp_lg_u64 vcc, 0
	s_cselect_b64 s[40:41], -1, 0
	s_cbranch_vccnz .LBB0_1342
.LBB0_1338:
	s_waitcnt lgkmcnt(0)
	v_and_b32_e32 v146, v146, v154
	v_and_b32_e32 v147, v147, v155
	v_and_b32_e32 v148, v148, v156
	v_and_b32_e32 v149, v149, v157
	v_lshlrev_b32_sdwa v248, s32, v225 dst_sel:DWORD dst_unused:UNUSED_PAD src0_sel:DWORD src1_sel:BYTE_1
	v_lshrrev_b32_sdwa v249, s11, v226 dst_sel:DWORD dst_unused:UNUSED_PAD src0_sel:DWORD src1_sel:BYTE_1
	ds_read_b64 v[154:155], v248 offset:51200
	ds_read_b64 v[156:157], v249 offset:51200
	s_waitcnt lgkmcnt(14)
	v_mfma_f32_32x32x16_bf16 v[20:35], v[146:149], v[114:117], v[20:35]
	v_exp_f32_e32 v86, v86
	v_exp_f32_e32 v87, v87
	v_exp_f32_e32 v88, v88
	v_exp_f32_e32 v89, v89
	s_waitcnt lgkmcnt(12)
	v_mfma_f32_32x32x16_bf16 v[4:19], v[146:149], v[110:113], v[4:19]
	v_mfma_f32_32x32x16_bf16 v[228:243], v[146:149], v[204:207], v[228:243]
	v_exp_f32_e32 v90, v90
	v_exp_f32_e32 v91, v91
	v_exp_f32_e32 v92, v92
	v_exp_f32_e32 v93, v93
	s_waitcnt lgkmcnt(0)
	v_and_b32_e32 v142, v142, v154
	v_and_b32_e32 v143, v143, v155
	v_and_b32_e32 v144, v144, v156
	v_and_b32_e32 v145, v145, v157
	v_lshlrev_b32_sdwa v248, s32, v225 dst_sel:DWORD dst_unused:UNUSED_PAD src0_sel:DWORD src1_sel:BYTE_2
	v_lshrrev_b32_sdwa v249, s11, v226 dst_sel:DWORD dst_unused:UNUSED_PAD src0_sel:DWORD src1_sel:BYTE_2
	ds_read_b64 v[154:155], v248 offset:51200
	ds_read_b64 v[156:157], v249 offset:51200
	s_waitcnt lgkmcnt(10)
	v_mfma_f32_32x32x16_bf16 v[20:35], v[142:145], v[106:109], v[20:35]
	v_exp_f32_e32 v94, v94
	v_exp_f32_e32 v95, v95
	v_exp_f32_e32 v96, v96
	v_exp_f32_e32 v97, v97
	s_waitcnt lgkmcnt(8)
	v_mfma_f32_32x32x16_bf16 v[4:19], v[142:145], v[102:105], v[4:19]
	v_mfma_f32_32x32x16_bf16 v[228:243], v[142:145], v[204:207], v[228:243]
	v_exp_f32_e32 v98, v98
	v_exp_f32_e32 v99, v99
	v_exp_f32_e32 v100, v100
	v_exp_f32_e32 v101, v101
	s_waitcnt lgkmcnt(0)
	v_and_b32_e32 v130, v130, v154
	v_and_b32_e32 v131, v131, v155
	v_and_b32_e32 v132, v132, v156
	v_and_b32_e32 v133, v133, v157
	v_lshlrev_b32_sdwa v248, s32, v225 dst_sel:DWORD dst_unused:UNUSED_PAD src0_sel:DWORD src1_sel:BYTE_3
	v_lshrrev_b32_sdwa v249, s11, v226 dst_sel:DWORD dst_unused:UNUSED_PAD src0_sel:DWORD src1_sel:BYTE_3
	ds_read_b64 v[154:155], v248 offset:51200
	ds_read_b64 v[156:157], v249 offset:51200
	s_waitcnt lgkmcnt(6)
	v_mfma_f32_32x32x16_bf16 v[20:35], v[130:133], v[80:83], v[20:35]
	v_exp_f32_e32 v36, v36
	v_exp_f32_e32 v37, v37
	v_exp_f32_e32 v38, v38
	v_exp_f32_e32 v39, v39
	s_waitcnt lgkmcnt(4)
	v_mfma_f32_32x32x16_bf16 v[4:19], v[130:133], v[76:79], v[4:19]
	v_mfma_f32_32x32x16_bf16 v[228:243], v[130:133], v[204:207], v[228:243]
	v_exp_f32_e32 v40, v40
	v_exp_f32_e32 v41, v41
	v_exp_f32_e32 v42, v42
	v_exp_f32_e32 v43, v43
	s_waitcnt lgkmcnt(0)
	v_and_b32_e32 v118, v118, v154
	v_and_b32_e32 v119, v119, v155
	v_and_b32_e32 v120, v120, v156
	v_and_b32_e32 v121, v121, v157
	s_nop 0
	s_waitcnt lgkmcnt(2)
	v_mfma_f32_32x32x16_bf16 v[20:35], v[118:121], v[72:75], v[20:35]
	v_exp_f32_e32 v44, v44
	v_exp_f32_e32 v45, v45
	v_exp_f32_e32 v46, v46
	v_exp_f32_e32 v47, v47
	s_waitcnt lgkmcnt(0)
	v_mfma_f32_32x32x16_bf16 v[4:19], v[118:121], v[68:71], v[4:19]
	v_mfma_f32_32x32x16_bf16 v[228:243], v[118:121], v[204:207], v[228:243]
	v_exp_f32_e32 v48, v48
	v_exp_f32_e32 v49, v49
	v_exp_f32_e32 v50, v50
	v_exp_f32_e32 v51, v51
	v_and_b32_e32 v225, 0x0f0f0f0f, v218
	v_and_b32_e32 v226, 0xf0f0f0f0, v218
	s_andn2_b64 vcc, exec, s[40:41]
	v_lshl_add_u32 v52, v214, 4, s57
	s_cbranch_vccnz .LBB0_1340
; #define SBAR() __builtin_amdgcn_sched_barrier(0)
;   #define RESC() do{ if(resc){ asm volatile("s_waitcnt lgkmcnt(0)":::"memory"); \
;       _Pragma("unroll") for(int d_=0;d_<2;++d_) _Pragma("unroll") for(int r=0;r<16;++r)o[d_][r]*=wsf[crow(r,hi)]; } }while(0)
;   #define PKW(P,B) cvtpk_s(P[B],P[B+1])
; __device__ __forceinline__ void pv(f32x16*o,int vb,bf16x8 pa0,bf16x8 pa1,bf16x8 pa2,bf16x8 pa3){
;   #pragma unroll
;   for(int d0=0;d0<2;++d0){s16x4 lo[4],hi[4];
;     #pragma unroll
;     for(int ks=0;ks<4;++ks){
;       asm volatile("ds_read_b64_tr_b16 %0,%1 offset:%c2":"=&v"(lo[ks]):"v"(vb),"i"(d0*4096+ks*1024):"memory");
;       asm volatile("ds_read_b64_tr_b16 %0,%1 offset:%c2":"=&v"(hi[ks]):"v"(vb),"i"(d0*4096+ks*1024+512):"memory");}
;     asm volatile("s_waitcnt lgkmcnt(0)":::"memory");SBAR();
;     ...
;     o[d0]=__builtin_amdgcn_mfma_f32_32x32x16_bf16(pa0,PK(0),o[d0],0,0,0);
;     o[d0]=__builtin_amdgcn_mfma_f32_32x32x16_bf16(pa1,PK(1),o[d0],0,0,0);
;     o[d0]=__builtin_amdgcn_mfma_f32_32x32x16_bf16(pa2,PK(2),o[d0],0,0,0);
;     o[d0]=__builtin_amdgcn_mfma_f32_32x32x16_bf16(pa3,PK(3),o[d0],0,0,0);
;     ...
;   }
; }
; template<int THRL> __device__ __forceinline__ void attn_unit(int b,int h,int qb,const bf16*Q,const bf16*__restrict__ K,const bf16*__restrict__ V,bf16*O,const unsigned*MASK,char*shm){
;     ...
;   STEP(pB0,pB1,pA0,pA1,NT-1,false,false,false,wB,wA); RESC();
;   { float sacc=pB0[0]+pB0[1]; _Pragma("unroll") for(int r=2;r<16;++r)sacc+=pB0[r]; _Pragma("unroll") for(int r=0;r<16;++r)sacc+=pB1[r]; l_reg+=sacc;
;     pw0=(u32x4){PKW(pB0,0),PKW(pB0,2),PKW(pB0,4),PKW(pB0,6)};pw1=(u32x4){PKW(pB0,8),PKW(pB0,10),PKW(pB0,12),PKW(pB0,14)};pw2=(u32x4){PKW(pB1,0),PKW(pB1,2),PKW(pB1,4),PKW(pB1,6)};pw3=(u32x4){PKW(pB1,8),PKW(pB1,10),PKW(pB1,12),PKW(pB1,14)};
;     SBAR(); pv(o,vb0+sl_cur,PAF(0),PAF(1),PAF(2),PAF(3)); }
;     ...
;   {auto rr=__builtin_amdgcn_permlane32_swap(__float_as_uint(l_reg),__float_as_uint(l_reg),false,false);l_reg=__uint_as_float(rr[0])+__uint_as_float(rr[1]);}
;   if(hi==0)wsf[32+r32]=l_reg;asm volatile("s_waitcnt lgkmcnt(0)":::"memory");
	s_waitcnt lgkmcnt(0)
	ds_read_b128 v[54:57], v52 offset:49248
	ds_read_b128 v[58:61], v52 offset:49216
	ds_read_b128 v[62:65], v52 offset:49184
	ds_read_b128 v[66:69], v52 offset:49152
	s_waitcnt lgkmcnt(3)
	v_pk_mul_f32 v[34:35], v[34:35], v[56:57]
	s_waitcnt lgkmcnt(2)
	v_pk_mul_f32 v[30:31], v[30:31], v[60:61]
	s_waitcnt lgkmcnt(1)
	v_pk_mul_f32 v[26:27], v[26:27], v[64:65]
	s_waitcnt lgkmcnt(0)
	v_pk_mul_f32 v[22:23], v[22:23], v[68:69]
	v_pk_mul_f32 v[32:33], v[32:33], v[54:55]
	v_pk_mul_f32 v[28:29], v[28:29], v[58:59]
	v_pk_mul_f32 v[24:25], v[24:25], v[62:63]
	v_pk_mul_f32 v[20:21], v[20:21], v[66:67]
	v_pk_mul_f32 v[18:19], v[18:19], v[56:57]
	v_pk_mul_f32 v[14:15], v[14:15], v[60:61]
	v_pk_mul_f32 v[10:11], v[10:11], v[64:65]
	v_pk_mul_f32 v[6:7], v[6:7], v[68:69]
	v_pk_mul_f32 v[16:17], v[16:17], v[54:55]
	v_pk_mul_f32 v[12:13], v[12:13], v[58:59]
	v_pk_mul_f32 v[8:9], v[8:9], v[62:63]
	v_pk_mul_f32 v[4:5], v[4:5], v[66:67]
	v_pk_mul_f32 v[242:243], v[242:243], v[56:57]
	v_pk_mul_f32 v[238:239], v[238:239], v[60:61]
	v_pk_mul_f32 v[234:235], v[234:235], v[64:65]
	v_pk_mul_f32 v[230:231], v[230:231], v[68:69]
	v_pk_mul_f32 v[240:241], v[240:241], v[54:55]
	v_pk_mul_f32 v[236:237], v[236:237], v[58:59]
	v_pk_mul_f32 v[232:233], v[232:233], v[62:63]
	v_pk_mul_f32 v[228:229], v[228:229], v[66:67]
.LBB0_1340:
	s_cmp_lg_u32 0, -1
	s_cselect_b32 s4, 0, 0
	s_addk_i32 s4, 0x6000
	v_cvt_pk_bf16_f32 v36, v36, v37
	v_add3_u32 v53, v217, s4, v215
	v_cvt_pk_bf16_f32 v54, v86, v87
	v_cvt_pk_bf16_f32 v55, v88, v89
	v_cvt_pk_bf16_f32 v56, v90, v91
	v_cvt_pk_bf16_f32 v57, v92, v93
	v_cvt_pk_bf16_f32 v58, v94, v95
	v_cvt_pk_bf16_f32 v59, v96, v97
	v_cvt_pk_bf16_f32 v60, v98, v99
	v_cvt_pk_bf16_f32 v61, v100, v101
	v_cvt_pk_bf16_f32 v37, v38, v39
	v_cvt_pk_bf16_f32 v38, v40, v41
	v_cvt_pk_bf16_f32 v39, v42, v43
	v_cvt_pk_bf16_f32 v40, v44, v45
	v_cvt_pk_bf16_f32 v41, v46, v47
	v_cvt_pk_bf16_f32 v42, v48, v49
	v_cvt_pk_bf16_f32 v43, v50, v51
	v_lshlrev_b32_sdwa v248, s32, v225 dst_sel:DWORD dst_unused:UNUSED_PAD src0_sel:DWORD src1_sel:BYTE_0
	v_lshrrev_b32_sdwa v249, s11, v226 dst_sel:DWORD dst_unused:UNUSED_PAD src0_sel:DWORD src1_sel:BYTE_0
	ds_read_b64 v[86:87], v248 offset:51200
	ds_read_b64 v[88:89], v249 offset:51200
	v_lshlrev_b32_sdwa v248, s32, v225 dst_sel:DWORD dst_unused:UNUSED_PAD src0_sel:DWORD src1_sel:BYTE_1
	v_lshrrev_b32_sdwa v249, s11, v226 dst_sel:DWORD dst_unused:UNUSED_PAD src0_sel:DWORD src1_sel:BYTE_1
	ds_read_b64 v[90:91], v248 offset:51200
	ds_read_b64 v[92:93], v249 offset:51200
	v_lshlrev_b32_sdwa v248, s32, v225 dst_sel:DWORD dst_unused:UNUSED_PAD src0_sel:DWORD src1_sel:BYTE_2
	v_lshrrev_b32_sdwa v249, s11, v226 dst_sel:DWORD dst_unused:UNUSED_PAD src0_sel:DWORD src1_sel:BYTE_2
	ds_read_b64 v[94:95], v248 offset:51200
	ds_read_b64 v[96:97], v249 offset:51200
	v_lshlrev_b32_sdwa v248, s32, v225 dst_sel:DWORD dst_unused:UNUSED_PAD src0_sel:DWORD src1_sel:BYTE_3
	v_lshrrev_b32_sdwa v249, s11, v226 dst_sel:DWORD dst_unused:UNUSED_PAD src0_sel:DWORD src1_sel:BYTE_3
	ds_read_b64 v[98:99], v248 offset:51200
	ds_read_b64 v[100:101], v249 offset:51200
	v_add3_u32 v53, v53, v216, s60
	ds_read_b64_tr_b16 v[44:45],v53 offset:0
	ds_read_b64_tr_b16 v[46:47],v53 offset:512
	ds_read_b64_tr_b16 v[48:49],v53 offset:1024
	ds_read_b64_tr_b16 v[50:51],v53 offset:1536
	ds_read_b64_tr_b16 v[62:63],v53 offset:2048
	ds_read_b64_tr_b16 v[64:65],v53 offset:2560
	ds_read_b64_tr_b16 v[66:67],v53 offset:3072
	ds_read_b64_tr_b16 v[68:69],v53 offset:3584
	s_waitcnt lgkmcnt(0)
	v_and_b32_e32 v54, v54, v86
	v_and_b32_e32 v55, v55, v87
	v_and_b32_e32 v56, v56, v88
	v_and_b32_e32 v57, v57, v89
	v_and_b32_e32 v58, v58, v90
	v_and_b32_e32 v59, v59, v91
	v_and_b32_e32 v60, v60, v92
	v_and_b32_e32 v61, v61, v93
	v_and_b32_e32 v36, v36, v94
	v_and_b32_e32 v37, v37, v95
	v_and_b32_e32 v38, v38, v96
	v_and_b32_e32 v39, v39, v97
	v_and_b32_e32 v40, v40, v98
	v_and_b32_e32 v41, v41, v99
	v_and_b32_e32 v42, v42, v100
	v_and_b32_e32 v43, v43, v101
	s_nop 0
	v_mfma_f32_32x32x16_bf16 v[20:35], v[54:57], v[44:47], v[20:35]
	ds_read_b64_tr_b16 v[44:45],v53 offset:4096
	ds_read_b64_tr_b16 v[46:47],v53 offset:4608
	v_mfma_f32_32x32x16_bf16 v[20:35], v[58:61], v[48:51], v[20:35]
	ds_read_b64_tr_b16 v[48:49],v53 offset:5120
	ds_read_b64_tr_b16 v[50:51],v53 offset:5632
	v_mfma_f32_32x32x16_bf16 v[20:35], v[36:39], v[62:65], v[20:35]
	ds_read_b64_tr_b16 v[62:63],v53 offset:6144
	ds_read_b64_tr_b16 v[64:65],v53 offset:6656
	v_mfma_f32_32x32x16_bf16 v[20:35], v[40:43], v[66:69], v[20:35]
	v_mfma_f32_32x32x16_bf16 v[228:243], v[54:57], v[204:207], v[228:243]
	v_mfma_f32_32x32x16_bf16 v[228:243], v[58:61], v[204:207], v[228:243]
	v_mfma_f32_32x32x16_bf16 v[228:243], v[36:39], v[204:207], v[228:243]
	v_mfma_f32_32x32x16_bf16 v[228:243], v[40:43], v[204:207], v[228:243]
	ds_read_b64_tr_b16 v[66:67],v53 offset:7168
	ds_read_b64_tr_b16 v[68:69],v53 offset:7680
	s_waitcnt lgkmcnt(0)
	v_mfma_f32_32x32x16_bf16 v[4:19], v[54:57], v[44:47], v[4:19]
	v_cmp_gt_u32_e32 vcc, 32, v1
	v_mfma_f32_32x32x16_bf16 v[4:19], v[58:61], v[48:51], v[4:19]
	v_mfma_f32_32x32x16_bf16 v[4:19], v[36:39], v[62:65], v[4:19]
	v_mov_b32_e32 v36, v2
	s_nop 1
	v_permlane32_swap_b32_e32 v2, v36
	v_mfma_f32_32x32x16_bf16 v[4:19], v[40:43], v[66:69], v[4:19]
	s_and_saveexec_b64 s[4:5], vcc
	s_cbranch_execz .LBB0_1260
	v_lshl_add_u32 v37, v213, 2, s57
	v_add_f32_e32 v2, v2, v36
	ds_write_b32 v37, v2 offset:49280
	s_branch .LBB0_1260
